# speedup vs baseline: 1.0179x; 1.0059x over previous
.LBB8_4:
	s_load_dwordx4 s[32:35], s[0:1], 0x18
	s_load_dword s36, s[0:1], 0x28
	s_load_dwordx4 s[4:7], s[0:1], 0x60
	s_load_dwordx2 s[14:15], s[0:1], 0x10
	s_ashr_i32 s2, s2, 3
	s_add_i32 s2, s3, s2
	s_abs_i32 s3, s2
	s_waitcnt lgkmcnt(0)
	s_mov_b32 s92, s6
	s_mov_b32 s93, s7
	v_cvt_f32_u32_e32 v72, s6
	v_cvt_f32_u32_e32 v73, s7
	v_cvt_f32_u32_e32 v74, s2
	v_rcp_iflag_f32_e32 v72, v72
	v_rcp_iflag_f32_e32 v73, v73
	v_add_f32_e32 v74, 0.5, v74
	s_nop 0
	v_mul_f32_e32 v74, v74, v72
	v_cvt_u32_f32_e32 v74, v74
	v_cvt_f32_u32_e32 v72, v74
	v_add_f32_e32 v72, 0.5, v72
	v_readfirstlane_b32 s94, v74
	v_mul_f32_e32 v72, v72, v73
	v_cvt_u32_f32_e32 v72, v72
	s_mul_i32 s90, s94, s92
	s_sub_i32 s90, s2, s90
	v_readfirstlane_b32 s95, v72
	s_nop 0
	s_mul_i32 s91, s95, s93
	s_sub_i32 s91, s94, s91
	s_mov_b32 s3, s94
	s_mov_b32 s18, s90
	s_mov_b32 s2, s95
	s_mov_b32 s3, s91
	v_lshrrev_b32_e32 v1, 6, v0
	v_lshrrev_b32_e32 v3, 2, v0
	v_mov_b32_e32 v17, 0
	v_and_b32_e32 v12, 31, v0
	v_lshlrev_b32_e32 v2, 3, v0
	s_mul_i32 s6, s2, s4
	s_lshl_b32 s16, s3, 6
	v_and_b32_e32 v16, 24, v2
	s_ashr_i32 s7, s6, 31
	v_or_b32_e32 v6, s16, v3
	s_ashr_i32 s17, s16, 31
	v_lshl_add_u64 v[4:5], s[6:7], 0, v[16:17]
	v_lshlrev_b32_e32 v2, 5, v1
	v_lshl_or_b32 v2, s18, 7, v2
	s_mul_i32 s19, s14, s17
	v_mad_u64_u32 v[4:5], s[2:3], s14, v6, v[4:5]
	v_mul_lo_u32 v6, s15, v6
	v_add3_u32 v5, v6, v5, s19
	v_or_b32_e32 v14, v2, v12
	v_lshlrev_b64 v[6:7], 1, v[4:5]
	v_ashrrev_i32_e32 v15, 31, v14
	v_lshl_add_u64 v[4:5], s[10:11], 0, v[6:7]
	v_lshl_add_u64 v[6:7], s[8:9], 0, v[6:7]
	v_lshl_add_u64 v[14:15], v[14:15], 2, s[12:13]
	global_load_dwordx4 v[78:81], v[6:7], off
	global_load_dwordx4 v[82:85], v[4:5], off
	global_load_dword v13, v[14:15], off
	s_load_dwordx2 s[2:3], s[0:1], 0x38
	s_movk_i32 s9, 0x50
	v_lshlrev_b32_e32 v16, 1, v16
	v_and_b32_e32 v14, 63, v0
	s_nop 7
	v_bfe_u32 v15, v0, 5, 1
	v_mad_u32_u24 v17, v3, s9, v16
	s_mov_b32 s10, s36
	s_lshr_b32 s7, s7, 28
	v_lshl_or_b32 v10, s18, 2, v1
	s_add_i32 s6, s6, s7
	s_ashr_i32 s6, s6, 4
	s_waitcnt lgkmcnt(0)
	s_ashr_i32 s18, s10, 31
	s_lshr_b32 s18, s18, 28
	s_ashr_i32 s8, s4, 31
	s_add_i32 s10, s10, s18
	s_ashr_i32 s7, s6, 31
	s_lshr_b32 s8, s8, 27
	s_ashr_i32 s10, s10, 4
	v_mov_b32_e32 v8, s6
	v_mov_b32_e32 v9, s7
	s_add_i32 s4, s4, s8
	v_mad_i64_i32 v[8:9], s[6:7], v10, s10, v[8:9]
	s_ashr_i32 s4, s4, 5
	v_lshlrev_b64 v[10:11], 10, v[8:9]
	s_add_i32 s8, s4, -1
	v_lshl_or_b32 v10, v14, 4, v10
	s_min_i32 s11, s8, 2
	v_lshl_add_u64 v[8:9], s[32:33], 0, v[10:11]
	global_load_dwordx4 v[30:33], v[6:7], off offset:64
	global_load_dwordx4 v[22:25], v[4:5], off offset:64
	v_lshl_add_u64 v[10:11], s[34:35], 0, v[10:11]
	global_load_dwordx4 v[38:41], v[8:9], off
	global_load_dwordx4 v[18:21], v[8:9], off offset:1024
	global_load_dwordx4 v[54:57], v[10:11], off
	global_load_dwordx4 v[26:29], v[10:11], off offset:1024
	global_load_dwordx4 v[42:45], v[8:9], off offset:2048
	global_load_dwordx4 v[50:53], v[10:11], off offset:2048
	s_lshl_b32 s6, s11, 5
	s_ashr_i32 s7, s6, 31
	s_lshl_b64 s[6:7], s[6:7], 1
	v_lshl_add_u64 v[60:61], v[6:7], 0, s[6:7]
	v_lshl_add_u64 v[58:59], v[4:5], 0, s[6:7]
	global_load_dwordx4 v[46:49], v[60:61], off
	global_load_dwordx4 v[34:37], v[58:59], off
	v_accvgpr_write_b32 a0, 0
	v_accvgpr_write_b32 a1, 0
	v_accvgpr_write_b32 a2, 0
	v_accvgpr_write_b32 a3, 0
	v_accvgpr_write_b32 a4, 0
	v_accvgpr_write_b32 a5, 0
	v_accvgpr_write_b32 a6, 0
	v_accvgpr_write_b32 a7, 0
	v_accvgpr_write_b32 a8, 0
	v_accvgpr_write_b32 a9, 0
	v_accvgpr_write_b32 a10, 0
	v_accvgpr_write_b32 a11, 0
	v_accvgpr_write_b32 a12, 0
	v_accvgpr_write_b32 a13, 0
	v_accvgpr_write_b32 a14, 0
	v_accvgpr_write_b32 a15, 0
	v_accvgpr_write_b32 a16, 0
	v_accvgpr_write_b32 a17, 0
	v_accvgpr_write_b32 a18, 0
	v_accvgpr_write_b32 a19, 0
	v_accvgpr_write_b32 a20, 0
	v_accvgpr_write_b32 a21, 0
	v_accvgpr_write_b32 a22, 0
	v_accvgpr_write_b32 a23, 0
	v_accvgpr_write_b32 a24, 0
	v_accvgpr_write_b32 a25, 0
	v_accvgpr_write_b32 a26, 0
	v_accvgpr_write_b32 a27, 0
	v_accvgpr_write_b32 a28, 0
	v_accvgpr_write_b32 a29, 0
	v_accvgpr_write_b32 a30, 0
	v_accvgpr_write_b32 a31, 0
	s_waitcnt vmcnt(12)
	ds_write_b128 v17, v[78:81]
	s_waitcnt vmcnt(11)
	ds_write_b128 v17, v[82:85] offset:5120
	s_waitcnt lgkmcnt(0)
	s_barrier
	v_mul_u32_u24_e32 v17, 0x50, v3
	v_lshlrev_b32_e32 v3, 4, v15
	v_mad_u32_u24 v70, v12, s9, v3
	ds_read_b128 v[58:61], v70 offset:2560
	ds_read_b128 v[66:69], v70
	ds_read_b128 v[62:65], v70 offset:7680
	ds_read_b128 v[70:73], v70 offset:5120
	v_mul_u32_u24_e32 v74, 0x50, v12
	s_mov_b32 s6, 4
	s_nop 7
	v_add_u32_e32 v3, v3, v74
	v_add_u32_e32 v16, v16, v17

.LBB8_7:
	s_load_dwordx2 s[0:1], s[0:1], 0x40
	s_waitcnt vmcnt(7)
	v_mul_u32_u24_e32 v40, 0x2400, v1
	v_accvgpr_read_b32 v39, a0
	v_accvgpr_read_b32 v38, a1
	v_lshl_or_b32 v1, v12, 2, v40
	s_waitcnt lgkmcnt(0)
	s_mul_hi_u32 s4, s0, s16
	s_mul_i32 s6, s0, s17
	s_add_i32 s4, s4, s6
	s_mul_i32 s6, s1, s16
	s_add_i32 s7, s4, s6
	s_movk_i32 s4, 0x240
	s_waitcnt vmcnt(2)
	v_accvgpr_read_b32 v37, a2
	v_accvgpr_read_b32 v36, a3
	s_waitcnt vmcnt(0)
	v_fma_f32 v12, s5, v39, v13
	v_mad_u32_u24 v1, v15, s4, v1
	v_fma_f32 v15, s5, v38, v13
	v_accvgpr_read_b32 v35, a4
	v_accvgpr_read_b32 v34, a5
	s_barrier
	ds_write2_b32 v1, v12, v15 offset1:36
	v_fma_f32 v12, s5, v37, v13
	v_fma_f32 v15, s5, v36, v13
	v_accvgpr_read_b32 v33, a6
	v_accvgpr_read_b32 v32, a7
	ds_write2_b32 v1, v12, v15 offset0:72 offset1:108
	v_fma_f32 v12, s5, v35, v13
	v_fma_f32 v15, s5, v34, v13
	v_add_u32_e32 v34, 0x400, v1
	v_accvgpr_read_b32 v31, a8
	v_accvgpr_read_b32 v30, a9
	ds_write2_b32 v34, v12, v15 offset0:32 offset1:68
	v_fma_f32 v12, s5, v33, v13
	v_fma_f32 v15, s5, v32, v13
	v_accvgpr_read_b32 v29, a10
	v_accvgpr_read_b32 v28, a11
	ds_write2_b32 v34, v12, v15 offset0:104 offset1:140
	v_fma_f32 v12, s5, v31, v13
	v_fma_f32 v15, s5, v30, v13
	v_add_u32_e32 v30, 0x800, v1
	v_accvgpr_read_b32 v27, a12
	v_accvgpr_read_b32 v26, a13
	ds_write2_b32 v30, v12, v15 offset0:64 offset1:100
	v_fma_f32 v12, s5, v29, v13
	v_fma_f32 v15, s5, v28, v13
	v_accvgpr_read_b32 v25, a14
	v_accvgpr_read_b32 v24, a15
	ds_write2_b32 v30, v12, v15 offset0:136 offset1:172
	v_fma_f32 v12, s5, v27, v13
	v_fma_f32 v15, s5, v26, v13
	v_add_u32_e32 v26, 0xc00, v1
	v_accvgpr_read_b32 v23, a16
	v_accvgpr_read_b32 v22, a17
	ds_write2_b32 v26, v12, v15 offset0:96 offset1:132
	v_fma_f32 v12, s5, v25, v13
	v_fma_f32 v15, s5, v24, v13
	v_accvgpr_read_b32 v21, a18
	v_accvgpr_read_b32 v20, a19
	ds_write2_b32 v26, v12, v15 offset0:168 offset1:204
	v_fma_f32 v12, s5, v23, v13
	v_fma_f32 v15, s5, v22, v13
	v_add_u32_e32 v22, 0x1000, v1
	v_accvgpr_read_b32 v19, a20
	v_accvgpr_read_b32 v18, a21
	ds_write2_b32 v22, v12, v15 offset0:128 offset1:164
	v_fma_f32 v12, s5, v21, v13
	v_fma_f32 v15, s5, v20, v13
	v_accvgpr_read_b32 v17, a22
	v_accvgpr_read_b32 v16, a23
	ds_write2_b32 v22, v12, v15 offset0:200 offset1:236
	v_fma_f32 v12, s5, v19, v13
	v_fma_f32 v15, s5, v18, v13
	v_add_u32_e32 v18, 0x1400, v1
	v_accvgpr_read_b32 v11, a24
	v_accvgpr_read_b32 v10, a25
	v_accvgpr_read_b32 v9, a26
	v_accvgpr_read_b32 v8, a27
	v_accvgpr_read_b32 v7, a28
	v_accvgpr_read_b32 v6, a29
	v_accvgpr_read_b32 v5, a30
	v_accvgpr_read_b32 v4, a31
	s_mul_i32 s6, s0, s16
	ds_write2_b32 v18, v12, v15 offset0:160 offset1:196
	v_fma_f32 v12, s5, v17, v13
	v_fma_f32 v15, s5, v16, v13
	v_add_u32_e32 v16, 0x1600, v1
	ds_write2_b32 v16, v12, v15 offset0:104 offset1:140
	v_fma_f32 v11, s5, v11, v13
	v_fma_f32 v10, s5, v10, v13
	v_add_u32_e32 v12, 0x1800, v1
	v_fma_f32 v9, s5, v9, v13
	v_fma_f32 v8, s5, v8, v13
	v_fma_f32 v7, s5, v7, v13
	v_fma_f32 v6, s5, v6, v13
	v_fma_f32 v5, s5, v5, v13
	v_fmac_f32_e32 v13, s5, v4
	s_lshl_b64 s[4:5], s[6:7], 2
	ds_write2_b32 v12, v11, v10 offset0:192 offset1:228
	v_add_u32_e32 v10, 0x1c00, v1
	s_add_u32 s2, s2, s4
	v_ashrrev_i32_e32 v3, 31, v2
	ds_write2_b32 v10, v9, v8 offset0:8 offset1:44
	v_add_u32_e32 v8, 0x1e00, v1
	v_add_u32_e32 v1, 0x2000, v1
	s_addc_u32 s3, s3, s5
	v_lshlrev_b32_e32 v0, 4, v0
	ds_write2_b32 v1, v5, v13 offset0:40 offset1:76
	v_lshl_add_u64 v[2:3], v[2:3], 2, s[2:3]
	v_and_b32_e32 v0, 0x70, v0
	v_mov_b32_e32 v1, 0
	ds_write2_b32 v8, v7, v6 offset0:96 offset1:132
	v_lshrrev_b32_e32 v12, 3, v14
	v_lshl_add_u64 v[8:9], v[2:3], 0, v[0:1]
	v_or_b32_e32 v0, v40, v0
	s_movk_i32 s2, 0x90
	v_mad_u32_u24 v13, v12, s2, v0
	ds_read_b128 v[0:3], v13
	v_mad_u64_u32 v[4:5], s[2:3], s0, v12, 0
	v_mov_b32_e32 v6, v5
	v_mad_u64_u32 v[6:7], s[2:3], s1, v12, v[6:7]
	v_mov_b32_e32 v5, v6
	v_lshl_add_u64 v[10:11], v[4:5], 2, v[8:9]
	ds_read_b128 v[4:7], v13 offset:1152
	s_waitcnt lgkmcnt(1)
	global_store_dwordx4 v[10:11], v[0:3], off sc1
	s_nop 1
	v_or_b32_e32 v3, 8, v12
	v_mad_u64_u32 v[0:1], s[2:3], s0, v3, 0
	v_mov_b32_e32 v2, v1
	v_mad_u64_u32 v[2:3], s[2:3], s1, v3, v[2:3]
	v_mov_b32_e32 v1, v2
	v_lshl_add_u64 v[0:1], v[0:1], 2, v[8:9]
	s_waitcnt lgkmcnt(0)
	global_store_dwordx4 v[0:1], v[4:7], off sc1
	ds_read_b128 v[0:3], v13 offset:2304
	s_nop 0
	v_or_b32_e32 v7, 16, v12
	v_mad_u64_u32 v[4:5], s[2:3], s0, v7, 0
	v_mov_b32_e32 v6, v5
	v_mad_u64_u32 v[6:7], s[2:3], s1, v7, v[6:7]
	v_mov_b32_e32 v5, v6
	v_lshl_add_u64 v[10:11], v[4:5], 2, v[8:9]
	ds_read_b128 v[4:7], v13 offset:3456
	s_waitcnt lgkmcnt(1)
	global_store_dwordx4 v[10:11], v[0:3], off sc1
	s_nop 1
	v_or_b32_e32 v3, 24, v12
	v_mad_u64_u32 v[0:1], s[2:3], s0, v3, 0
	v_mov_b32_e32 v2, v1
	v_mad_u64_u32 v[2:3], s[2:3], s1, v3, v[2:3]
	v_mov_b32_e32 v1, v2
	v_lshl_add_u64 v[0:1], v[0:1], 2, v[8:9]
	s_waitcnt lgkmcnt(0)
	global_store_dwordx4 v[0:1], v[4:7], off sc1
	ds_read_b128 v[0:3], v13 offset:4608
	s_nop 0
	v_or_b32_e32 v7, 32, v12
	v_mad_u64_u32 v[4:5], s[2:3], s0, v7, 0
	v_mov_b32_e32 v6, v5
	v_mad_u64_u32 v[6:7], s[2:3], s1, v7, v[6:7]
	v_mov_b32_e32 v5, v6
	v_lshl_add_u64 v[10:11], v[4:5], 2, v[8:9]
	ds_read_b128 v[4:7], v13 offset:5760
	s_waitcnt lgkmcnt(1)
	global_store_dwordx4 v[10:11], v[0:3], off sc1
	s_nop 1
	v_or_b32_e32 v3, 40, v12
	v_mad_u64_u32 v[0:1], s[2:3], s0, v3, 0
	v_mov_b32_e32 v2, v1
	v_mad_u64_u32 v[2:3], s[2:3], s1, v3, v[2:3]
	v_mov_b32_e32 v1, v2
	v_lshl_add_u64 v[0:1], v[0:1], 2, v[8:9]
	s_waitcnt lgkmcnt(0)
	global_store_dwordx4 v[0:1], v[4:7], off sc1
	ds_read_b128 v[0:3], v13 offset:6912
	s_nop 0
	v_or_b32_e32 v7, 48, v12
	v_mad_u64_u32 v[4:5], s[2:3], s0, v7, 0
	v_mov_b32_e32 v6, v5
	v_mad_u64_u32 v[6:7], s[2:3], s1, v7, v[6:7]
	v_mov_b32_e32 v5, v6
	v_lshl_add_u64 v[10:11], v[4:5], 2, v[8:9]
	ds_read_b128 v[4:7], v13 offset:8064
	s_waitcnt lgkmcnt(1)
	global_store_dwordx4 v[10:11], v[0:3], off sc1
	s_nop 1
	v_or_b32_e32 v3, 56, v12
	v_mad_u64_u32 v[0:1], s[2:3], s0, v3, 0
	v_mov_b32_e32 v2, v1
	v_mad_u64_u32 v[2:3], s[0:1], s1, v3, v[2:3]
	v_mov_b32_e32 v1, v2
	v_lshl_add_u64 v[0:1], v[0:1], 2, v[8:9]
	s_waitcnt lgkmcnt(0)
	global_store_dwordx4 v[0:1], v[4:7], off sc1
	s_endpgm
	s_endpgm
	s_endpgm
	s_endpgm
	s_endpgm
	s_endpgm
	s_endpgm
	s_endpgm
	s_endpgm
	s_endpgm
	s_endpgm
	s_endpgm
	s_endpgm
	s_endpgm
	s_endpgm
	s_endpgm
	s_endpgm
	s_endpgm
	s_endpgm
	s_endpgm
	s_endpgm
	s_endpgm
	s_endpgm
	s_endpgm
	s_endpgm
	s_endpgm
	s_endpgm
	s_endpgm
	s_endpgm
	s_endpgm
	s_endpgm
	s_endpgm
	s_endpgm
	s_endpgm
	s_endpgm
	s_endpgm
	s_endpgm
	s_endpgm
	s_endpgm
	s_endpgm
	s_endpgm
	s_endpgm
	s_endpgm
	s_endpgm
	s_endpgm
	s_endpgm
	s_endpgm
	s_endpgm
	s_endpgm
	s_endpgm
	s_endpgm
	s_endpgm
	s_endpgm
	s_endpgm
	s_endpgm
	s_endpgm
	s_endpgm
	s_endpgm
	s_endpgm
	s_endpgm
	s_endpgm

.LBB9_4:
	s_load_dwordx4 s[32:35], s[0:1], 0x18
	s_load_dword s36, s[0:1], 0x28
	s_load_dwordx4 s[4:7], s[0:1], 0x60
	s_load_dwordx2 s[12:13], s[0:1], 0x10
	s_ashr_i32 s2, s2, 3
	s_add_i32 s2, s3, s2
	s_abs_i32 s3, s2
	s_waitcnt lgkmcnt(0)
	s_lshl_b32 s26, s7, 7
	s_lshl_b32 s24, s26, 5
	s_mov_b32 s27, 0
	s_cmp_eq_u32 s12, 0x800
	s_cselect_b32 s25, s24, 32
	s_cselect_b32 s26, s26, 1
	s_cselect_b32 s12, 32, s12
	s_mov_b32 s92, s6
	s_mov_b32 s93, s7
	v_cvt_f32_u32_e32 v100, s6
	v_cvt_f32_u32_e32 v101, s7
	v_cvt_f32_u32_e32 v102, s2
	v_rcp_iflag_f32_e32 v100, v100
	v_rcp_iflag_f32_e32 v101, v101
	v_add_f32_e32 v102, 0.5, v102
	s_nop 0
	v_mul_f32_e32 v102, v102, v100
	v_cvt_u32_f32_e32 v102, v102
	v_cvt_f32_u32_e32 v100, v102
	v_add_f32_e32 v100, 0.5, v100
	v_readfirstlane_b32 s94, v102
	v_mul_f32_e32 v100, v100, v101
	v_cvt_u32_f32_e32 v100, v100
	s_mul_i32 s90, s94, s92
	s_sub_i32 s90, s2, s90
	v_readfirstlane_b32 s95, v100
	s_nop 0
	s_mul_i32 s91, s95, s93
	s_sub_i32 s91, s94, s91
	s_mov_b32 s3, s94
	s_mov_b32 s14, s90
	s_mov_b32 s16, s95
	s_mov_b32 s2, s91
	v_lshlrev_b32_e32 v3, 3, v0
	v_lshrrev_b32_e32 v2, 2, v0
	v_and_b32_e32 v8, 24, v3
	v_mov_b32_e32 v9, 0
	v_lshlrev_b32_e32 v3, 1, v8
	v_lshrrev_b32_e32 v23, 6, v0
	v_and_b32_e32 v22, 31, v0
	s_lshl_b32 s15, s2, 7
	s_mul_i32 s2, s16, s4
	s_mul_i32 s26, s2, s26
	s_ashr_i32 s3, s2, 31
	v_or_b32_e32 v1, s15, v2
	s_ashr_i32 s17, s15, 31
	v_lshl_add_u64 v[4:5], s[26:27], 0, v[8:9]
	s_mul_i32 s20, s12, s17
	v_mad_u64_u32 v[4:5], s[18:19], s12, v1, v[4:5]
	v_mul_lo_u32 v1, s13, v1
	s_lshl_b64 s[6:7], s[12:13], 6
	v_add3_u32 v5, v1, v5, s20
	v_lshl_add_u64 v[6:7], v[4:5], 0, s[6:7]
	v_lshlrev_b64 v[4:5], 1, v[4:5]
	v_lshl_add_u64 v[12:13], s[10:11], 0, v[4:5]
	v_lshl_add_u64 v[14:15], s[8:9], 0, v[4:5]
	s_lshl_b64 s[6:7], s[12:13], 7
	v_lshl_add_u64 v[10:11], v[6:7], 1, s[8:9]
	v_lshl_add_u64 v[16:17], v[12:13], 0, s[6:7]
	global_load_dwordx4 v[124:127], v[14:15], off
	global_load_dwordx4 v[128:131], v[12:13], off
	global_load_dwordx4 v[132:135], v[10:11], off
	global_load_dwordx4 v[136:139], v[16:17], off
	s_load_dwordx2 s[6:7], s[0:1], 0x38
	s_movk_i32 s9, 0x50
	v_and_b32_e32 v1, 63, v0
	s_nop 7
	v_bfe_u32 v24, v0, 5, 1
	v_mad_u32_u24 v112, v2, s9, v3
	s_mov_b32 s10, s36
	s_lshr_b32 s3, s3, 28
	s_ashr_i32 s8, s4, 31
	s_add_i32 s2, s2, s3
	s_lshr_b32 s8, s8, 27
	s_waitcnt lgkmcnt(0)
	s_ashr_i32 s12, s10, 31
	s_lshr_b32 s12, s12, 28
	s_ashr_i32 s2, s2, 4
	s_add_i32 s4, s4, s8
	s_add_i32 s10, s10, s12
	s_ashr_i32 s3, s2, 31
	s_ashr_i32 s4, s4, 5
	v_lshl_or_b32 v6, s14, 2, v23
	s_ashr_i32 s10, s10, 4
	v_mov_b32_e32 v4, s2
	v_mov_b32_e32 v5, s3
	s_add_i32 s8, s4, -1
	v_mad_i64_i32 v[4:5], s[2:3], v6, s10, v[4:5]
	s_min_i32 s11, s8, 2
	v_lshlrev_b64 v[4:5], 10, v[4:5]
	v_lshl_or_b32 v4, v1, 4, v4
	s_mul_i32 s2, s11, s25
	v_lshl_add_u64 v[18:19], s[32:33], 0, v[4:5]
	s_ashr_i32 s3, s2, 31
	s_lshl_b32 s28, s25, 1
	s_mov_b32 s29, 0
	v_lshl_add_u64 v[116:117], v[14:15], 0, s[28:29]
	v_lshl_add_u64 v[118:119], v[12:13], 0, s[28:29]
	v_lshl_add_u64 v[120:121], v[10:11], 0, s[28:29]
	v_lshl_add_u64 v[122:123], v[16:17], 0, s[28:29]
	global_load_dwordx4 v[44:47], v[116:117], off
	global_load_dwordx4 v[48:51], v[118:119], off
	global_load_dwordx4 v[32:35], v[120:121], off
	global_load_dwordx4 v[28:31], v[122:123], off
	v_lshl_add_u64 v[20:21], s[34:35], 0, v[4:5]
	global_load_dwordx4 v[64:67], v[18:19], off
	global_load_dwordx4 v[36:39], v[18:19], off offset:1024
	global_load_dwordx4 v[80:83], v[20:21], off
	global_load_dwordx4 v[40:43], v[20:21], off offset:1024
	global_load_dwordx4 v[68:71], v[18:19], off offset:2048
	global_load_dwordx4 v[76:79], v[20:21], off offset:2048
	s_lshl_b64 s[2:3], s[2:3], 1
	v_lshl_add_u64 v[26:27], v[14:15], 0, s[2:3]
	v_lshl_add_u64 v[4:5], v[10:11], 0, s[2:3]
	v_lshl_add_u64 v[6:7], v[12:13], 0, s[2:3]
	v_lshl_add_u64 v[8:9], v[16:17], 0, s[2:3]
	global_load_dwordx4 v[60:63], v[26:27], off
	global_load_dwordx4 v[56:59], v[4:5], off
	global_load_dwordx4 v[72:75], v[6:7], off
	global_load_dwordx4 v[52:55], v[8:9], off
	v_accvgpr_write_b32 a48, 0
	v_accvgpr_write_b32 a49, 0
	v_accvgpr_write_b32 a50, 0
	v_accvgpr_write_b32 a51, 0
	v_accvgpr_write_b32 a52, 0
	v_accvgpr_write_b32 a53, 0
	v_accvgpr_write_b32 a54, 0
	v_accvgpr_write_b32 a55, 0
	v_accvgpr_write_b32 a56, 0
	v_accvgpr_write_b32 a57, 0
	v_accvgpr_write_b32 a58, 0
	v_accvgpr_write_b32 a59, 0
	v_accvgpr_write_b32 a60, 0
	v_accvgpr_write_b32 a61, 0
	v_accvgpr_write_b32 a62, 0
	v_accvgpr_write_b32 a63, 0
	v_accvgpr_write_b32 a32, 0
	v_accvgpr_write_b32 a33, 0
	v_accvgpr_write_b32 a34, 0
	v_accvgpr_write_b32 a35, 0
	v_accvgpr_write_b32 a36, 0
	v_accvgpr_write_b32 a37, 0
	v_accvgpr_write_b32 a38, 0
	v_accvgpr_write_b32 a39, 0
	v_accvgpr_write_b32 a40, 0
	v_accvgpr_write_b32 a41, 0
	v_accvgpr_write_b32 a42, 0
	v_accvgpr_write_b32 a43, 0
	v_accvgpr_write_b32 a44, 0
	v_accvgpr_write_b32 a45, 0
	v_accvgpr_write_b32 a46, 0
	v_accvgpr_write_b32 a47, 0
	v_accvgpr_write_b32 a16, 0
	v_accvgpr_write_b32 a17, 0
	v_accvgpr_write_b32 a18, 0
	v_accvgpr_write_b32 a19, 0
	v_accvgpr_write_b32 a20, 0
	v_accvgpr_write_b32 a21, 0
	v_accvgpr_write_b32 a22, 0
	v_accvgpr_write_b32 a23, 0
	v_accvgpr_write_b32 a24, 0
	v_accvgpr_write_b32 a25, 0
	v_accvgpr_write_b32 a26, 0
	v_accvgpr_write_b32 a27, 0
	v_accvgpr_write_b32 a28, 0
	v_accvgpr_write_b32 a29, 0
	v_accvgpr_write_b32 a30, 0
	v_accvgpr_write_b32 a31, 0
	v_accvgpr_write_b32 a0, 0
	v_accvgpr_write_b32 a1, 0
	v_accvgpr_write_b32 a2, 0
	v_accvgpr_write_b32 a3, 0
	v_accvgpr_write_b32 a4, 0
	v_accvgpr_write_b32 a5, 0
	v_accvgpr_write_b32 a6, 0
	v_accvgpr_write_b32 a7, 0
	v_accvgpr_write_b32 a8, 0
	v_accvgpr_write_b32 a9, 0
	v_accvgpr_write_b32 a10, 0
	v_accvgpr_write_b32 a11, 0
	v_accvgpr_write_b32 a12, 0
	v_accvgpr_write_b32 a13, 0
	v_accvgpr_write_b32 a14, 0
	v_accvgpr_write_b32 a15, 0
	s_waitcnt vmcnt(17)
	ds_write_b128 v112, v[124:127]
	s_waitcnt vmcnt(16)
	ds_write_b128 v112, v[128:131] offset:10240
	s_waitcnt vmcnt(15)
	ds_write_b128 v112, v[132:135] offset:5120
	s_waitcnt vmcnt(14)
	ds_write_b128 v112, v[136:139] offset:15360
	s_waitcnt lgkmcnt(0)
	s_barrier
	v_lshlrev_b32_e32 v4, 4, v24
	v_mad_u32_u24 v6, v22, s9, v4
	ds_read_b128 v[84:87], v6 offset:7680
	ds_read_b128 v[92:95], v6 offset:5120
	ds_read_b128 v[88:91], v6 offset:17920
	ds_read_b128 v[96:99], v6 offset:15360
	ds_read_b128 v[100:103], v6 offset:2560
	ds_read_b128 v[104:107], v6
	ds_read_b128 v[108:111], v6 offset:12800
	ds_read_b128 v[112:115], v6 offset:10240
	v_mul_u32_u24_e32 v2, 0x50, v2
	v_mul_u32_u24_e32 v5, 0x50, v22
	s_mov_b32 s2, 4
	s_nop 7
	v_add_u32_e32 v25, v4, v5
	v_add_u32_e32 v26, v3, v2

.LBB9_7:
	s_load_dwordx4 s[0:3], s[0:1], 0x40
	s_ashr_i32 s4, s16, 31
	s_waitcnt vmcnt(1)
	v_lshlrev_b32_e32 v69, 5, v23
	v_lshl_or_b32 v70, s14, 7, v69
	v_mul_u32_u24_e32 v23, 0x2400, v23
	s_waitcnt lgkmcnt(0)
	s_mul_hi_u32 s8, s2, s16
	s_mul_i32 s4, s2, s4
	s_add_i32 s4, s8, s4
	s_mul_i32 s3, s3, s16
	s_add_i32 s3, s4, s3
	s_mul_i32 s2, s2, s16
	s_lshl_b64 s[2:3], s[2:3], 2
	s_add_u32 s4, s6, s2
	s_addc_u32 s6, s7, s3
	s_mul_hi_u32 s2, s0, s15
	s_mul_i32 s3, s0, s17
	s_add_i32 s2, s2, s3
	s_mul_i32 s3, s1, s15
	s_add_i32 s3, s2, s3
	s_mul_i32 s2, s0, s15
	s_lshl_b64 s[2:3], s[2:3], 2
	s_add_u32 s2, s4, s2
	s_addc_u32 s3, s6, s3
	v_ashrrev_i32_e32 v71, 31, v70
	v_lshlrev_b32_e32 v0, 4, v0
	v_accvgpr_read_b32 v68, a0
	v_accvgpr_read_b32 v67, a1
	v_lshl_add_u64 v[70:71], v[70:71], 2, s[2:3]
	v_and_b32_e32 v72, 0x70, v0
	v_mov_b32_e32 v73, 0
	v_lshl_or_b32 v22, v22, 2, v23
	s_movk_i32 s2, 0x240
	v_accvgpr_read_b32 v66, a2
	v_lshrrev_b32_e32 v69, 3, v1
	v_lshl_add_u64 v[0:1], v[70:71], 0, v[72:73]
	v_or_b32_e32 v70, v23, v72
	v_fma_f32 v23, s5, v68, 0
	v_mad_u32_u24 v68, v24, s2, v22
	v_fma_f32 v22, s5, v67, 0
	v_accvgpr_read_b32 v65, a3
	s_barrier
	ds_write_b32 v68, v22 offset:144
	v_fma_f32 v22, s5, v66, 0
	v_accvgpr_read_b32 v64, a4
	ds_write_b32 v68, v22 offset:288
	v_fma_f32 v22, s5, v65, 0
	v_accvgpr_read_b32 v63, a5
	ds_write_b32 v68, v22 offset:432
	v_fma_f32 v22, s5, v64, 0
	v_accvgpr_read_b32 v62, a6
	ds_write_b32 v68, v22 offset:1152
	v_fma_f32 v22, s5, v63, 0
	v_accvgpr_read_b32 v61, a7
	ds_write_b32 v68, v22 offset:1296
	v_fma_f32 v22, s5, v62, 0
	v_accvgpr_read_b32 v60, a8
	ds_write_b32 v68, v22 offset:1440
	v_fma_f32 v22, s5, v61, 0
	v_accvgpr_read_b32 v59, a9
	ds_write_b32 v68, v22 offset:1584
	v_fma_f32 v22, s5, v60, 0
	v_accvgpr_read_b32 v58, a10
	ds_write_b32 v68, v22 offset:2304
	v_fma_f32 v22, s5, v59, 0
	v_accvgpr_read_b32 v57, a11
	ds_write_b32 v68, v22 offset:2448
	v_fma_f32 v22, s5, v58, 0
	v_accvgpr_read_b32 v56, a12
	ds_write_b32 v68, v22 offset:2592
	v_fma_f32 v22, s5, v57, 0
	v_accvgpr_read_b32 v55, a13
	ds_write_b32 v68, v22 offset:2736
	v_fma_f32 v22, s5, v56, 0
	v_accvgpr_read_b32 v54, a14
	ds_write_b32 v68, v22 offset:3456
	v_fma_f32 v22, s5, v55, 0
	v_accvgpr_read_b32 v53, a15
	ds_write_b32 v68, v22 offset:3600
	v_fma_f32 v22, s5, v54, 0
	v_accvgpr_read_b32 v52, a16
	ds_write_b32 v68, v22 offset:3744
	v_fma_f32 v22, s5, v53, 0
	v_accvgpr_read_b32 v51, a17
	ds_write_b32 v68, v22 offset:3888
	v_fma_f32 v22, s5, v52, 0
	v_accvgpr_read_b32 v50, a18
	ds_write_b32 v68, v22 offset:4608
	v_fma_f32 v22, s5, v51, 0
	v_accvgpr_read_b32 v49, a19
	ds_write_b32 v68, v22 offset:4752
	v_fma_f32 v22, s5, v50, 0
	v_accvgpr_read_b32 v48, a20
	ds_write_b32 v68, v22 offset:4896
	v_fma_f32 v22, s5, v49, 0
	v_accvgpr_read_b32 v47, a21
	ds_write_b32 v68, v22 offset:5040
	v_fma_f32 v22, s5, v48, 0
	v_accvgpr_read_b32 v46, a22
	ds_write_b32 v68, v22 offset:5760
	v_fma_f32 v22, s5, v47, 0
	v_accvgpr_read_b32 v45, a23
	ds_write_b32 v68, v22 offset:5904
	v_fma_f32 v22, s5, v46, 0
	v_accvgpr_read_b32 v44, a24
	ds_write_b32 v68, v22 offset:6048
	v_fma_f32 v22, s5, v45, 0
	v_accvgpr_read_b32 v43, a25
	ds_write_b32 v68, v22 offset:6192
	v_fma_f32 v22, s5, v44, 0
	v_accvgpr_read_b32 v42, a26
	ds_write_b32 v68, v22 offset:6912
	v_fma_f32 v22, s5, v43, 0
	v_accvgpr_read_b32 v41, a27
	ds_write_b32 v68, v22 offset:7056
	v_fma_f32 v22, s5, v42, 0
	v_accvgpr_read_b32 v40, a28
	ds_write_b32 v68, v22 offset:7200
	v_fma_f32 v22, s5, v41, 0
	v_accvgpr_read_b32 v39, a29
	ds_write_b32 v68, v22 offset:7344
	v_fma_f32 v22, s5, v40, 0
	v_accvgpr_read_b32 v38, a30
	ds_write_b32 v68, v22 offset:8064
	v_fma_f32 v22, s5, v39, 0
	v_accvgpr_read_b32 v37, a31
	ds_write_b32 v68, v22 offset:8208
	v_fma_f32 v22, s5, v38, 0
	s_movk_i32 s4, 0x90
	ds_write_b32 v68, v22 offset:8352
	v_fma_f32 v22, s5, v37, 0
	v_mad_u32_u24 v71, v69, s4, v70
	ds_write_b32 v68, v23
	ds_write_b32 v68, v22 offset:8496
	ds_read_b128 v[38:41], v71
	v_mad_u64_u32 v[22:23], s[2:3], s0, v69, 0
	v_accvgpr_read_b32 v25, a43
	v_mov_b32_e32 v24, v23
	v_mad_u64_u32 v[42:43], s[2:3], s1, v69, v[24:25]
	v_mov_b32_e32 v23, v42
	v_or_b32_e32 v37, 8, v69
	v_lshl_add_u64 v[22:23], v[22:23], 2, v[0:1]
	v_mad_u32_u24 v46, v37, s4, v70
	ds_read_b128 v[42:45], v46
	s_waitcnt lgkmcnt(1)
	global_store_dwordx4 v[22:23], v[38:41], off sc1
	v_mad_u64_u32 v[22:23], s[2:3], s0, v37, 0
	v_mov_b32_e32 v24, v23
	v_mad_u64_u32 v[38:39], s[2:3], s1, v37, v[24:25]
	v_mov_b32_e32 v23, v38
	v_lshl_add_u64 v[22:23], v[22:23], 2, v[0:1]
	v_or_b32_e32 v37, 16, v69
	ds_read_b128 v[38:41], v46 offset:1152
	s_waitcnt lgkmcnt(1)
	global_store_dwordx4 v[22:23], v[42:45], off sc1
	v_mad_u64_u32 v[22:23], s[2:3], s0, v37, 0
	v_mov_b32_e32 v24, v23
	v_mad_u64_u32 v[42:43], s[2:3], s1, v37, v[24:25]
	v_mov_b32_e32 v23, v42
	v_lshl_add_u64 v[22:23], v[22:23], 2, v[0:1]
	v_or_b32_e32 v37, 24, v69
	ds_read_b128 v[42:45], v46 offset:2304
	s_waitcnt lgkmcnt(1)
	global_store_dwordx4 v[22:23], v[38:41], off sc1
	v_mad_u64_u32 v[22:23], s[2:3], s0, v37, 0
	v_mov_b32_e32 v24, v23
	v_mad_u64_u32 v[38:39], s[2:3], s1, v37, v[24:25]
	v_mov_b32_e32 v23, v38
	v_lshl_add_u64 v[22:23], v[22:23], 2, v[0:1]
	v_or_b32_e32 v37, 32, v69
	ds_read_b128 v[38:41], v46 offset:3456
	s_waitcnt lgkmcnt(1)
	global_store_dwordx4 v[22:23], v[42:45], off sc1
	v_mad_u64_u32 v[22:23], s[2:3], s0, v37, 0
	v_mov_b32_e32 v24, v23
	v_mad_u64_u32 v[42:43], s[2:3], s1, v37, v[24:25]
	v_mov_b32_e32 v23, v42
	v_lshl_add_u64 v[22:23], v[22:23], 2, v[0:1]
	v_or_b32_e32 v37, 40, v69
	ds_read_b128 v[42:45], v46 offset:4608
	s_waitcnt lgkmcnt(1)
	global_store_dwordx4 v[22:23], v[38:41], off sc1
	v_mad_u64_u32 v[22:23], s[2:3], s0, v37, 0
	v_mov_b32_e32 v24, v23
	v_mad_u64_u32 v[38:39], s[2:3], s1, v37, v[24:25]
	v_mov_b32_e32 v23, v38
	v_lshl_add_u64 v[22:23], v[22:23], 2, v[0:1]
	v_or_b32_e32 v37, 48, v69
	ds_read_b128 v[38:41], v46 offset:5760
	s_waitcnt lgkmcnt(1)
	global_store_dwordx4 v[22:23], v[42:45], off sc1
	v_mad_u64_u32 v[22:23], s[2:3], s0, v37, 0
	v_mov_b32_e32 v24, v23
	v_mad_u64_u32 v[42:43], s[2:3], s1, v37, v[24:25]
	v_mov_b32_e32 v23, v42
	v_lshl_add_u64 v[22:23], v[22:23], 2, v[0:1]
	v_or_b32_e32 v37, 56, v69
	ds_read_b128 v[42:45], v46 offset:6912
	s_waitcnt lgkmcnt(1)
	global_store_dwordx4 v[22:23], v[38:41], off sc1
	v_mad_u64_u32 v[22:23], s[2:3], s0, v37, 0
	v_mov_b32_e32 v24, v23
	v_mad_u64_u32 v[38:39], s[2:3], s1, v37, v[24:25]
	v_mov_b32_e32 v23, v38
	v_accvgpr_read_b32 v36, a32
	v_lshl_add_u64 v[22:23], v[22:23], 2, v[0:1]
	v_accvgpr_read_b32 v35, a33
	s_waitcnt lgkmcnt(0)
	global_store_dwordx4 v[22:23], v[42:45], off sc1
	v_fma_f32 v22, s5, v36, 0
	v_accvgpr_read_b32 v34, a34
	ds_write_b32 v68, v22
	v_fma_f32 v22, s5, v35, 0
	v_accvgpr_read_b32 v33, a35
	ds_write_b32 v68, v22 offset:144
	v_fma_f32 v22, s5, v34, 0
	v_accvgpr_read_b32 v32, a36
	ds_write_b32 v68, v22 offset:288
	v_fma_f32 v22, s5, v33, 0
	v_accvgpr_read_b32 v31, a37
	ds_write_b32 v68, v22 offset:432
	v_fma_f32 v22, s5, v32, 0
	v_accvgpr_read_b32 v30, a38
	ds_write_b32 v68, v22 offset:1152
	v_fma_f32 v22, s5, v31, 0
	v_accvgpr_read_b32 v29, a39
	ds_write_b32 v68, v22 offset:1296
	v_fma_f32 v22, s5, v30, 0
	v_accvgpr_read_b32 v28, a40
	ds_write_b32 v68, v22 offset:1440
	v_fma_f32 v22, s5, v29, 0
	v_accvgpr_read_b32 v27, a41
	ds_write_b32 v68, v22 offset:1584
	v_fma_f32 v22, s5, v28, 0
	v_accvgpr_read_b32 v26, a42
	ds_write_b32 v68, v22 offset:2304
	v_fma_f32 v22, s5, v27, 0
	v_accvgpr_read_b32 v17, a48
	v_accvgpr_read_b32 v16, a49
	v_accvgpr_read_b32 v15, a50
	v_accvgpr_read_b32 v14, a51
	v_accvgpr_read_b32 v13, a52
	v_accvgpr_read_b32 v12, a53
	v_accvgpr_read_b32 v11, a54
	v_accvgpr_read_b32 v10, a55
	v_accvgpr_read_b32 v9, a56
	v_accvgpr_read_b32 v8, a57
	v_accvgpr_read_b32 v7, a58
	v_accvgpr_read_b32 v6, a59
	v_accvgpr_read_b32 v5, a60
	v_accvgpr_read_b32 v4, a61
	v_accvgpr_read_b32 v3, a62
	v_accvgpr_read_b32 v2, a63
	v_accvgpr_read_b32 v21, a44
	v_accvgpr_read_b32 v20, a45
	v_accvgpr_read_b32 v19, a46
	v_accvgpr_read_b32 v18, a47
	ds_write_b32 v68, v22 offset:2448
	v_fma_f32 v22, s5, v26, 0
	ds_write_b32 v68, v22 offset:2592
	v_fma_f32 v22, s5, v25, 0
	v_fma_f32 v21, s5, v21, 0
	v_fma_f32 v20, s5, v20, 0
	v_fma_f32 v19, s5, v19, 0
	v_fma_f32 v18, s5, v18, 0
	v_fma_f32 v17, s5, v17, 0
	v_fma_f32 v16, s5, v16, 0
	v_fma_f32 v15, s5, v15, 0
	v_fma_f32 v14, s5, v14, 0
	v_fma_f32 v13, s5, v13, 0
	v_fma_f32 v12, s5, v12, 0
	v_fma_f32 v11, s5, v11, 0
	v_fma_f32 v10, s5, v10, 0
	v_fma_f32 v9, s5, v9, 0
	v_fma_f32 v8, s5, v8, 0
	v_fma_f32 v7, s5, v7, 0
	v_fma_f32 v6, s5, v6, 0
	v_fma_f32 v5, s5, v5, 0
	v_fma_f32 v4, s5, v4, 0
	v_fma_f32 v3, s5, v3, 0
	v_fma_f32 v2, s5, v2, 0
	ds_write_b32 v68, v22 offset:2736
	ds_write_b32 v68, v21 offset:3456
	ds_write_b32 v68, v20 offset:3600
	ds_write_b32 v68, v19 offset:3744
	ds_write_b32 v68, v18 offset:3888
	ds_write_b32 v68, v17 offset:4608
	ds_write_b32 v68, v16 offset:4752
	ds_write_b32 v68, v15 offset:4896
	ds_write_b32 v68, v14 offset:5040
	ds_write_b32 v68, v13 offset:5760
	ds_write_b32 v68, v12 offset:5904
	ds_write_b32 v68, v11 offset:6048
	ds_write_b32 v68, v10 offset:6192
	ds_write_b32 v68, v9 offset:6912
	ds_write_b32 v68, v8 offset:7056
	ds_write_b32 v68, v7 offset:7200
	ds_write_b32 v68, v6 offset:7344
	ds_write_b32 v68, v5 offset:8064
	ds_write_b32 v68, v4 offset:8208
	ds_write_b32 v68, v3 offset:8352
	ds_write_b32 v68, v2 offset:8496
	v_or_b32_e32 v9, 64, v69
	ds_read_b128 v[2:5], v71
	v_mad_u64_u32 v[6:7], s[2:3], s0, v9, 0
	v_mov_b32_e32 v8, v7
	v_mad_u64_u32 v[8:9], s[2:3], s1, v9, v[8:9]
	v_mov_b32_e32 v7, v8
	v_lshl_add_u64 v[10:11], v[6:7], 2, v[0:1]
	ds_read_b128 v[6:9], v46
	s_waitcnt lgkmcnt(1)
	global_store_dwordx4 v[10:11], v[2:5], off sc1
	s_nop 1
	v_or_b32_e32 v5, 0x48, v69
	v_mad_u64_u32 v[2:3], s[2:3], s0, v5, 0
	v_mov_b32_e32 v4, v3
	v_mad_u64_u32 v[4:5], s[2:3], s1, v5, v[4:5]
	v_mov_b32_e32 v3, v4
	v_lshl_add_u64 v[2:3], v[2:3], 2, v[0:1]
	s_waitcnt lgkmcnt(0)
	global_store_dwordx4 v[2:3], v[6:9], off sc1
	ds_read_b128 v[2:5], v46 offset:1152
	s_nop 0
	v_or_b32_e32 v9, 0x50, v69
	v_mad_u64_u32 v[6:7], s[2:3], s0, v9, 0
	v_mov_b32_e32 v8, v7
	v_mad_u64_u32 v[8:9], s[2:3], s1, v9, v[8:9]
	v_mov_b32_e32 v7, v8
	v_lshl_add_u64 v[10:11], v[6:7], 2, v[0:1]
	ds_read_b128 v[6:9], v46 offset:2304
	s_waitcnt lgkmcnt(1)
	global_store_dwordx4 v[10:11], v[2:5], off sc1
	s_nop 1
	v_or_b32_e32 v5, 0x58, v69
	v_mad_u64_u32 v[2:3], s[2:3], s0, v5, 0
	v_mov_b32_e32 v4, v3
	v_mad_u64_u32 v[4:5], s[2:3], s1, v5, v[4:5]
	v_mov_b32_e32 v3, v4
	v_lshl_add_u64 v[2:3], v[2:3], 2, v[0:1]
	s_waitcnt lgkmcnt(0)
	global_store_dwordx4 v[2:3], v[6:9], off sc1
	ds_read_b128 v[2:5], v46 offset:3456
	s_nop 0
	v_or_b32_e32 v9, 0x60, v69
	v_mad_u64_u32 v[6:7], s[2:3], s0, v9, 0
	v_mov_b32_e32 v8, v7
	v_mad_u64_u32 v[8:9], s[2:3], s1, v9, v[8:9]
	v_mov_b32_e32 v7, v8
	v_lshl_add_u64 v[10:11], v[6:7], 2, v[0:1]
	ds_read_b128 v[6:9], v46 offset:4608
	s_waitcnt lgkmcnt(1)
	global_store_dwordx4 v[10:11], v[2:5], off sc1
	s_nop 1
	v_or_b32_e32 v5, 0x68, v69
	v_mad_u64_u32 v[2:3], s[2:3], s0, v5, 0
	v_mov_b32_e32 v4, v3
	v_mad_u64_u32 v[4:5], s[2:3], s1, v5, v[4:5]
	v_mov_b32_e32 v3, v4
	v_lshl_add_u64 v[2:3], v[2:3], 2, v[0:1]
	s_waitcnt lgkmcnt(0)
	global_store_dwordx4 v[2:3], v[6:9], off sc1
	ds_read_b128 v[2:5], v46 offset:5760
	s_nop 0
	v_or_b32_e32 v9, 0x70, v69
	v_mad_u64_u32 v[6:7], s[2:3], s0, v9, 0
	v_mov_b32_e32 v8, v7
	v_mad_u64_u32 v[8:9], s[2:3], s1, v9, v[8:9]
	v_mov_b32_e32 v7, v8
	v_lshl_add_u64 v[10:11], v[6:7], 2, v[0:1]
	ds_read_b128 v[6:9], v46 offset:6912
	s_waitcnt lgkmcnt(1)
	global_store_dwordx4 v[10:11], v[2:5], off sc1
	s_nop 1
	v_or_b32_e32 v5, 0x78, v69
	v_mad_u64_u32 v[2:3], s[2:3], s0, v5, 0
	v_mov_b32_e32 v4, v3
	v_mad_u64_u32 v[4:5], s[0:1], s1, v5, v[4:5]
	v_mov_b32_e32 v3, v4
	v_lshl_add_u64 v[0:1], v[2:3], 2, v[0:1]
	s_waitcnt lgkmcnt(0)
	global_store_dwordx4 v[0:1], v[6:9], off sc1
	s_endpgm
	s_endpgm
	s_endpgm
	s_endpgm
	s_endpgm
	s_endpgm
	s_endpgm
	s_endpgm
	s_endpgm
	s_endpgm
	s_endpgm
	.section	.rodata,"a",@progbits
	.p2align	6, 0x0

.LBB10_4:
	s_load_dwordx4 s[32:35], s[0:1], 0x18
	s_load_dword s36, s[0:1], 0x28
	s_load_dwordx4 s[4:7], s[0:1], 0x60
	s_load_dwordx2 s[12:13], s[0:1], 0x10
	s_ashr_i32 s2, s2, 3
	s_add_i32 s2, s3, s2
	s_abs_i32 s3, s2
	s_waitcnt lgkmcnt(0)
	s_lshl_b32 s26, s7, 6
	s_lshl_b32 s24, s26, 5
	s_mov_b32 s27, 0
	s_cmp_eq_u32 s12, 0x800
	s_cselect_b32 s25, s24, 32
	s_cselect_b32 s26, s26, 1
	s_cselect_b32 s12, 32, s12
	s_mov_b32 s92, s6
	s_mov_b32 s93, s7
	v_cvt_f32_u32_e32 v72, s6
	v_cvt_f32_u32_e32 v73, s7
	v_cvt_f32_u32_e32 v74, s2
	v_rcp_iflag_f32_e32 v72, v72
	v_rcp_iflag_f32_e32 v73, v73
	v_add_f32_e32 v74, 0.5, v74
	s_nop 0
	v_mul_f32_e32 v74, v74, v72
	v_cvt_u32_f32_e32 v74, v74
	v_cvt_f32_u32_e32 v72, v74
	v_add_f32_e32 v72, 0.5, v72
	v_readfirstlane_b32 s94, v74
	v_mul_f32_e32 v72, v72, v73
	v_cvt_u32_f32_e32 v72, v72
	s_mul_i32 s90, s94, s92
	s_sub_i32 s90, s2, s90
	v_readfirstlane_b32 s95, v72
	s_nop 0
	s_mul_i32 s91, s95, s93
	s_sub_i32 s91, s94, s91
	s_mov_b32 s3, s94
	s_mov_b32 s14, s90
	s_mov_b32 s16, s95
	s_mov_b32 s2, s91
	v_lshlrev_b32_e32 v2, 3, v0
	v_lshrrev_b32_e32 v13, 2, v0
	v_and_b32_e32 v14, 24, v2
	v_mov_b32_e32 v15, 0
	v_lshrrev_b32_e32 v11, 6, v0
	v_and_b32_e32 v10, 31, v0
	s_lshl_b32 s15, s2, 6
	s_mul_i32 s2, s16, s4
	s_mul_i32 s26, s2, s26
	s_ashr_i32 s3, s2, 31
	v_or_b32_e32 v1, s15, v13
	s_ashr_i32 s17, s15, 31
	v_lshl_add_u64 v[2:3], s[26:27], 0, v[14:15]
	s_mul_i32 s18, s12, s17
	v_mad_u64_u32 v[2:3], s[6:7], s12, v1, v[2:3]
	v_mul_lo_u32 v1, s13, v1
	v_add3_u32 v3, v1, v3, s18
	v_lshlrev_b64 v[4:5], 1, v[2:3]
	v_lshl_add_u64 v[2:3], s[10:11], 0, v[4:5]
	v_lshl_add_u64 v[4:5], s[8:9], 0, v[4:5]
	global_load_dwordx4 v[76:79], v[4:5], off
	global_load_dwordx4 v[88:91], v[2:3], off
	s_load_dwordx2 s[6:7], s[0:1], 0x38
	s_movk_i32 s9, 0x50
	v_lshlrev_b32_e32 v14, 1, v14
	v_and_b32_e32 v1, 63, v0
	s_nop 7
	v_bfe_u32 v12, v0, 5, 1
	v_mad_u32_u24 v15, v13, s9, v14
	s_mov_b32 s10, s36
	s_lshr_b32 s3, s3, 28
	s_add_i32 s2, s2, s3
	s_ashr_i32 s2, s2, 4
	s_ashr_i32 s8, s4, 31
	s_waitcnt lgkmcnt(0)
	s_ashr_i32 s12, s10, 31
	s_lshr_b32 s12, s12, 28
	s_add_i32 s10, s10, s12
	s_ashr_i32 s3, s2, 31
	s_lshr_b32 s8, s8, 27
	v_lshl_or_b32 v8, s14, 2, v11
	s_ashr_i32 s10, s10, 4
	v_mov_b32_e32 v6, s2
	v_mov_b32_e32 v7, s3
	s_add_i32 s4, s4, s8
	v_mad_i64_i32 v[6:7], s[2:3], v8, s10, v[6:7]
	s_ashr_i32 s4, s4, 5
	v_lshlrev_b64 v[8:9], 10, v[6:7]
	s_add_i32 s8, s4, -1
	v_lshl_or_b32 v8, v1, 4, v8
	s_min_i32 s11, s8, 2
	v_lshl_add_u64 v[6:7], s[32:33], 0, v[8:9]
	s_lshl_b32 s28, s25, 1
	s_mov_b32 s29, 0
	v_lshl_add_u64 v[72:73], v[4:5], 0, s[28:29]
	v_lshl_add_u64 v[74:75], v[2:3], 0, s[28:29]
	global_load_dwordx4 v[28:31], v[72:73], off
	global_load_dwordx4 v[20:23], v[74:75], off
	v_lshl_add_u64 v[8:9], s[34:35], 0, v[8:9]
	global_load_dwordx4 v[36:39], v[6:7], off
	global_load_dwordx4 v[16:19], v[6:7], off offset:1024
	global_load_dwordx4 v[52:55], v[8:9], off
	global_load_dwordx4 v[24:27], v[8:9], off offset:1024
	global_load_dwordx4 v[40:43], v[6:7], off offset:2048
	global_load_dwordx4 v[48:51], v[8:9], off offset:2048
	s_mul_i32 s2, s11, s25
	s_ashr_i32 s3, s2, 31
	s_lshl_b64 s[2:3], s[2:3], 1
	v_lshl_add_u64 v[58:59], v[4:5], 0, s[2:3]
	v_lshl_add_u64 v[56:57], v[2:3], 0, s[2:3]
	global_load_dwordx4 v[44:47], v[58:59], off
	global_load_dwordx4 v[32:35], v[56:57], off
	v_accvgpr_write_b32 a0, 0
	v_accvgpr_write_b32 a1, 0
	v_accvgpr_write_b32 a2, 0
	v_accvgpr_write_b32 a3, 0
	v_accvgpr_write_b32 a4, 0
	v_accvgpr_write_b32 a5, 0
	v_accvgpr_write_b32 a6, 0
	v_accvgpr_write_b32 a7, 0
	v_accvgpr_write_b32 a8, 0
	v_accvgpr_write_b32 a9, 0
	v_accvgpr_write_b32 a10, 0
	v_accvgpr_write_b32 a11, 0
	v_accvgpr_write_b32 a12, 0
	v_accvgpr_write_b32 a13, 0
	v_accvgpr_write_b32 a14, 0
	v_accvgpr_write_b32 a15, 0
	v_accvgpr_write_b32 a16, 0
	v_accvgpr_write_b32 a17, 0
	v_accvgpr_write_b32 a18, 0
	v_accvgpr_write_b32 a19, 0
	v_accvgpr_write_b32 a20, 0
	v_accvgpr_write_b32 a21, 0
	v_accvgpr_write_b32 a22, 0
	v_accvgpr_write_b32 a23, 0
	v_accvgpr_write_b32 a24, 0
	v_accvgpr_write_b32 a25, 0
	v_accvgpr_write_b32 a26, 0
	v_accvgpr_write_b32 a27, 0
	v_accvgpr_write_b32 a28, 0
	v_accvgpr_write_b32 a29, 0
	v_accvgpr_write_b32 a30, 0
	v_accvgpr_write_b32 a31, 0
	s_waitcnt vmcnt(11)
	ds_write_b128 v15, v[76:79]
	s_waitcnt vmcnt(10)
	ds_write_b128 v15, v[88:91] offset:5120
	s_waitcnt lgkmcnt(0)
	s_barrier
	v_mul_u32_u24_e32 v15, 0x50, v13
	v_lshlrev_b32_e32 v13, 4, v12
	v_mad_u32_u24 v68, v10, s9, v13
	ds_read_b128 v[56:59], v68 offset:2560
	ds_read_b128 v[64:67], v68
	ds_read_b128 v[60:63], v68 offset:7680
	ds_read_b128 v[68:71], v68 offset:5120
	v_mul_u32_u24_e32 v72, 0x50, v10
	s_mov_b32 s2, 4
	s_nop 7
	v_add_u32_e32 v13, v13, v72
	v_add_u32_e32 v14, v14, v15

.LBB10_7:
	s_load_dwordx4 s[0:3], s[0:1], 0x40
	s_ashr_i32 s4, s16, 31
	s_waitcnt vmcnt(7)
	v_lshlrev_b32_e32 v37, 5, v11
	v_lshl_or_b32 v38, s14, 7, v37
	v_mul_u32_u24_e32 v37, 0x2400, v11
	s_waitcnt lgkmcnt(0)
	s_mul_hi_u32 s8, s2, s16
	s_mul_i32 s4, s2, s4
	s_add_i32 s4, s8, s4
	s_mul_i32 s3, s3, s16
	s_add_i32 s3, s4, s3
	s_mul_hi_u32 s4, s0, s15
	s_mul_i32 s8, s0, s17
	s_add_i32 s4, s4, s8
	s_mul_i32 s8, s1, s15
	v_accvgpr_read_b32 v36, a0
	s_waitcnt vmcnt(2)
	v_accvgpr_read_b32 v35, a1
	s_add_i32 s9, s4, s8
	v_lshl_or_b32 v10, v10, 2, v37
	s_movk_i32 s4, 0x240
	v_accvgpr_read_b32 v34, a2
	v_accvgpr_read_b32 v33, a3
	v_fma_f32 v36, s5, v36, 0
	v_mad_u32_u24 v10, v12, s4, v10
	v_fma_f32 v12, s5, v35, 0
	v_accvgpr_read_b32 v32, a4
	v_accvgpr_read_b32 v31, a5
	s_barrier
	ds_write2_b32 v10, v36, v12 offset1:36
	v_fma_f32 v12, s5, v34, 0
	v_fma_f32 v33, s5, v33, 0
	v_accvgpr_read_b32 v30, a6
	v_accvgpr_read_b32 v29, a7
	ds_write2_b32 v10, v12, v33 offset0:72 offset1:108
	v_fma_f32 v12, s5, v32, 0
	v_fma_f32 v31, s5, v31, 0
	v_add_u32_e32 v32, 0x400, v10
	v_accvgpr_read_b32 v28, a8
	v_accvgpr_read_b32 v27, a9
	ds_write2_b32 v32, v12, v31 offset0:32 offset1:68
	v_fma_f32 v12, s5, v30, 0
	v_fma_f32 v29, s5, v29, 0
	v_accvgpr_read_b32 v26, a10
	v_accvgpr_read_b32 v25, a11
	ds_write2_b32 v32, v12, v29 offset0:104 offset1:140
	v_fma_f32 v12, s5, v28, 0
	v_fma_f32 v27, s5, v27, 0
	v_add_u32_e32 v28, 0x800, v10
	v_accvgpr_read_b32 v24, a12
	v_accvgpr_read_b32 v23, a13
	ds_write2_b32 v28, v12, v27 offset0:64 offset1:100
	v_fma_f32 v12, s5, v26, 0
	v_fma_f32 v25, s5, v25, 0
	v_accvgpr_read_b32 v22, a14
	v_accvgpr_read_b32 v21, a15
	ds_write2_b32 v28, v12, v25 offset0:136 offset1:172
	v_fma_f32 v12, s5, v24, 0
	v_fma_f32 v23, s5, v23, 0
	v_add_u32_e32 v24, 0xc00, v10
	v_accvgpr_read_b32 v20, a16
	v_accvgpr_read_b32 v19, a17
	ds_write2_b32 v24, v12, v23 offset0:96 offset1:132
	v_fma_f32 v12, s5, v22, 0
	v_fma_f32 v21, s5, v21, 0
	v_accvgpr_read_b32 v18, a18
	v_accvgpr_read_b32 v17, a19
	ds_write2_b32 v24, v12, v21 offset0:168 offset1:204
	v_fma_f32 v12, s5, v20, 0
	v_fma_f32 v19, s5, v19, 0
	v_add_u32_e32 v20, 0x1000, v10
	v_accvgpr_read_b32 v16, a20
	v_accvgpr_read_b32 v15, a21
	ds_write2_b32 v20, v12, v19 offset0:128 offset1:164
	v_fma_f32 v12, s5, v18, 0
	v_fma_f32 v17, s5, v17, 0
	v_accvgpr_read_b32 v14, a22
	v_accvgpr_read_b32 v13, a23
	s_mul_i32 s2, s2, s16
	ds_write2_b32 v20, v12, v17 offset0:200 offset1:236
	v_fma_f32 v12, s5, v16, 0
	v_fma_f32 v15, s5, v15, 0
	v_add_u32_e32 v16, 0x1400, v10
	v_accvgpr_read_b32 v9, a24
	v_accvgpr_read_b32 v8, a25
	ds_write2_b32 v16, v12, v15 offset0:160 offset1:196
	v_fma_f32 v12, s5, v14, 0
	v_fma_f32 v13, s5, v13, 0
	v_add_u32_e32 v14, 0x1600, v10
	s_lshl_b64 s[2:3], s[2:3], 2
	v_accvgpr_read_b32 v7, a26
	v_accvgpr_read_b32 v6, a27
	v_accvgpr_read_b32 v5, a28
	v_accvgpr_read_b32 v4, a29
	v_accvgpr_read_b32 v3, a30
	v_accvgpr_read_b32 v2, a31
	s_mul_i32 s8, s0, s15
	ds_write2_b32 v14, v12, v13 offset0:104 offset1:140
	v_fma_f32 v9, s5, v9, 0
	v_fma_f32 v8, s5, v8, 0
	v_add_u32_e32 v12, 0x1800, v10
	s_add_u32 s4, s6, s2
	ds_write2_b32 v12, v9, v8 offset0:192 offset1:228
	v_fma_f32 v7, s5, v7, 0
	v_fma_f32 v6, s5, v6, 0
	v_add_u32_e32 v8, 0x1c00, v10
	v_fma_f32 v5, s5, v5, 0
	v_fma_f32 v4, s5, v4, 0
	v_fma_f32 v3, s5, v3, 0
	v_fma_f32 v2, s5, v2, 0
	s_addc_u32 s5, s7, s3
	s_lshl_b64 s[2:3], s[8:9], 2
	ds_write2_b32 v8, v7, v6 offset0:8 offset1:44
	v_add_u32_e32 v6, 0x1e00, v10
	s_add_u32 s2, s4, s2
	v_lshlrev_b32_e32 v0, 4, v0
	v_ashrrev_i32_e32 v39, 31, v38
	ds_write2_b32 v6, v5, v4 offset0:96 offset1:132
	v_add_u32_e32 v4, 0x2000, v10
	s_addc_u32 s3, s5, s3
	v_and_b32_e32 v10, 0x70, v0
	ds_write2_b32 v4, v3, v2 offset0:40 offset1:76
	v_lshrrev_b32_e32 v12, 3, v1
	v_lshl_add_u64 v[2:3], v[38:39], 2, s[2:3]
	v_or_b32_e32 v0, v37, v10
	s_movk_i32 s2, 0x90
	v_mov_b32_e32 v11, 0
	v_mad_u32_u24 v13, v12, s2, v0
	v_lshl_add_u64 v[8:9], v[2:3], 0, v[10:11]
	ds_read_b128 v[0:3], v13
	v_mad_u64_u32 v[4:5], s[2:3], s0, v12, 0
	v_mov_b32_e32 v6, v5
	v_mad_u64_u32 v[6:7], s[2:3], s1, v12, v[6:7]
	v_mov_b32_e32 v5, v6
	v_lshl_add_u64 v[10:11], v[4:5], 2, v[8:9]
	ds_read_b128 v[4:7], v13 offset:1152
	s_waitcnt lgkmcnt(1)
	global_store_dwordx4 v[10:11], v[0:3], off sc1
	s_nop 1
	v_or_b32_e32 v3, 8, v12
	v_mad_u64_u32 v[0:1], s[2:3], s0, v3, 0
	v_mov_b32_e32 v2, v1
	v_mad_u64_u32 v[2:3], s[2:3], s1, v3, v[2:3]
	v_mov_b32_e32 v1, v2
	v_lshl_add_u64 v[0:1], v[0:1], 2, v[8:9]
	s_waitcnt lgkmcnt(0)
	global_store_dwordx4 v[0:1], v[4:7], off sc1
	ds_read_b128 v[0:3], v13 offset:2304
	s_nop 0
	v_or_b32_e32 v7, 16, v12
	v_mad_u64_u32 v[4:5], s[2:3], s0, v7, 0
	v_mov_b32_e32 v6, v5
	v_mad_u64_u32 v[6:7], s[2:3], s1, v7, v[6:7]
	v_mov_b32_e32 v5, v6
	v_lshl_add_u64 v[10:11], v[4:5], 2, v[8:9]
	ds_read_b128 v[4:7], v13 offset:3456
	s_waitcnt lgkmcnt(1)
	global_store_dwordx4 v[10:11], v[0:3], off sc1
	s_nop 1
	v_or_b32_e32 v3, 24, v12
	v_mad_u64_u32 v[0:1], s[2:3], s0, v3, 0
	v_mov_b32_e32 v2, v1
	v_mad_u64_u32 v[2:3], s[2:3], s1, v3, v[2:3]
	v_mov_b32_e32 v1, v2
	v_lshl_add_u64 v[0:1], v[0:1], 2, v[8:9]
	s_waitcnt lgkmcnt(0)
	global_store_dwordx4 v[0:1], v[4:7], off sc1
	ds_read_b128 v[0:3], v13 offset:4608
	s_nop 0
	v_or_b32_e32 v7, 32, v12
	v_mad_u64_u32 v[4:5], s[2:3], s0, v7, 0
	v_mov_b32_e32 v6, v5
	v_mad_u64_u32 v[6:7], s[2:3], s1, v7, v[6:7]
	v_mov_b32_e32 v5, v6
	v_lshl_add_u64 v[10:11], v[4:5], 2, v[8:9]
	ds_read_b128 v[4:7], v13 offset:5760
	s_waitcnt lgkmcnt(1)
	global_store_dwordx4 v[10:11], v[0:3], off sc1
	s_nop 1
	v_or_b32_e32 v3, 40, v12
	v_mad_u64_u32 v[0:1], s[2:3], s0, v3, 0
	v_mov_b32_e32 v2, v1
	v_mad_u64_u32 v[2:3], s[2:3], s1, v3, v[2:3]
	v_mov_b32_e32 v1, v2
	v_lshl_add_u64 v[0:1], v[0:1], 2, v[8:9]
	s_waitcnt lgkmcnt(0)
	global_store_dwordx4 v[0:1], v[4:7], off sc1
	ds_read_b128 v[0:3], v13 offset:6912
	s_nop 0
	v_or_b32_e32 v7, 48, v12
	v_mad_u64_u32 v[4:5], s[2:3], s0, v7, 0
	v_mov_b32_e32 v6, v5
	v_mad_u64_u32 v[6:7], s[2:3], s1, v7, v[6:7]
	v_mov_b32_e32 v5, v6
	v_lshl_add_u64 v[10:11], v[4:5], 2, v[8:9]
	ds_read_b128 v[4:7], v13 offset:8064
	s_waitcnt lgkmcnt(1)
	global_store_dwordx4 v[10:11], v[0:3], off sc1
	s_nop 1
	v_or_b32_e32 v3, 56, v12
	v_mad_u64_u32 v[0:1], s[2:3], s0, v3, 0
	v_mov_b32_e32 v2, v1
	v_mad_u64_u32 v[2:3], s[0:1], s1, v3, v[2:3]
	v_mov_b32_e32 v1, v2
	v_lshl_add_u64 v[0:1], v[0:1], 2, v[8:9]
	s_waitcnt lgkmcnt(0)
	global_store_dwordx4 v[0:1], v[4:7], off sc1
	s_endpgm
	s_endpgm
	s_endpgm
	s_endpgm
	s_endpgm
	s_endpgm
	s_endpgm
	s_endpgm
	s_endpgm
	s_endpgm
	s_endpgm
	s_endpgm
	s_endpgm
	s_endpgm
	s_endpgm
	s_endpgm
	s_endpgm
	s_endpgm
	s_endpgm
	s_endpgm
	s_endpgm
	s_endpgm
	s_endpgm
	s_endpgm
	s_endpgm
	s_endpgm
	s_endpgm
	s_endpgm
	s_endpgm
	s_endpgm
	s_endpgm
	s_endpgm
	s_endpgm
	s_endpgm
	s_endpgm
	s_endpgm
	s_endpgm
	s_endpgm
	s_endpgm
	s_endpgm
	s_endpgm
	s_endpgm
	s_endpgm
	s_endpgm

.LBB11_4:
	s_load_dwordx4 s[4:7], s[0:1], 0x60
	s_load_dword s16, s[0:1], 0x70
	s_ashr_i32 s2, s2, 3
	s_add_i32 s18, s3, s2
	s_abs_i32 s2, s18
	s_waitcnt lgkmcnt(0)
	s_load_dwordx2 s[2:3], s[0:1], 0x10
	s_load_dword s21, s[0:1], 0x28
	s_mov_b32 s92, s7
	s_mov_b32 s93, s16
	v_cvt_f32_u32_e32 v80, s7
	v_cvt_f32_u32_e32 v81, s16
	v_cvt_f32_u32_e32 v82, s18
	v_rcp_iflag_f32_e32 v80, v80
	v_rcp_iflag_f32_e32 v81, v81
	v_add_f32_e32 v82, 0.5, v82
	s_nop 0
	v_mul_f32_e32 v82, v82, v80
	v_cvt_u32_f32_e32 v82, v82
	v_cvt_f32_u32_e32 v80, v82
	v_add_f32_e32 v80, 0.5, v80
	v_readfirstlane_b32 s94, v82
	v_mul_f32_e32 v80, v80, v81
	v_cvt_u32_f32_e32 v80, v80
	s_mul_i32 s90, s94, s92
	s_sub_i32 s90, s18, s90
	v_readfirstlane_b32 s95, v80
	s_nop 0
	s_mul_i32 s7, s95, s93
	s_mov_b32 s19, s94
	s_mov_b32 s18, s90
	s_mov_b32 s17, s95
	v_lshrrev_b32_e32 v13, 2, v0
	v_mov_b32_e32 v31, 0
	v_lshrrev_b32_e32 v10, 1, v0
	v_and_b32_e32 v11, 32, v13
	s_lshl_b32 s16, s18, 6
	v_lshlrev_b32_e32 v1, 3, v0
	s_mul_i32 s18, s17, s5
	s_sub_i32 s7, s19, s7
	v_and_b32_e32 v30, 24, v1
	s_ashr_i32 s19, s18, 31
	s_lshl_b32 s7, s7, 6
	v_lshl_add_u64 v[2:3], s[18:19], 0, v[30:31]
	v_or_b32_e32 v4, s16, v13
	s_add_i32 s18, s4, -1
	v_or_b32_e32 v1, s7, v13
	s_ashr_i32 s20, s7, 31
	v_min_i32_e32 v6, s18, v4
	s_waitcnt lgkmcnt(0)
	s_mul_i32 s20, s2, s20
	v_mad_u64_u32 v[4:5], s[18:19], s2, v1, v[2:3]
	v_mul_lo_u32 v1, s3, v1
	v_mad_i64_i32 v[6:7], s[2:3], v6, s21, v[2:3]
	v_add3_u32 v5, v1, v5, s20
	v_lshlrev_b64 v[6:7], 1, v[6:7]
	v_lshlrev_b64 v[8:9], 1, v[4:5]
	v_lshl_add_u64 v[4:5], s[12:13], 0, v[6:7]
	global_load_dwordx4 v[64:67], v[4:5], off
	v_lshl_add_u64 v[6:7], s[14:15], 0, v[6:7]
	v_lshl_add_u64 v[2:3], s[8:9], 0, v[8:9]
	global_load_dwordx4 v[68:71], v[6:7], off
	global_load_dwordx4 v[72:75], v[2:3], off
	v_lshl_add_u64 v[8:9], s[10:11], 0, v[8:9]
	global_load_dwordx4 v[76:79], v[8:9], off
	s_load_dwordx2 s[8:9], s[0:1], 0x38
	v_mul_u32_u24_e32 v13, 40, v13
	v_lshlrev_b32_e32 v30, 1, v30
	s_mov_b32 s2, 0
	v_and_b32_e32 v1, 31, v0
	s_nop 7
	v_bfe_u32 v12, v0, 5, 1
	v_and_b32_e32 v10, 32, v10
	v_lshl_add_u32 v13, v13, 1, v30
	s_ashr_i32 s3, s5, 31
	s_lshr_b32 s3, s3, 27
	s_add_i32 s3, s5, s3
	s_ashr_i32 s3, s3, 5
	s_add_i32 s5, s3, -1
	s_min_i32 s10, s5, 2
	s_lshl_b32 s10, s10, 5
	s_ashr_i32 s11, s10, 31
	s_lshl_b64 s[10:11], s[10:11], 1
	v_lshl_add_u64 v[14:15], v[2:3], 0, s[10:11]
	global_load_dwordx4 v[16:19], v[2:3], off offset:64
	global_load_dwordx4 v[20:23], v[8:9], off offset:64
	global_load_dwordx4 v[24:27], v[4:5], off offset:64
	global_load_dwordx4 v[32:35], v[6:7], off offset:64
	global_load_dwordx4 v[28:31], v[14:15], off
	v_lshl_add_u64 v[14:15], v[8:9], 0, s[10:11]
	global_load_dwordx4 v[36:39], v[14:15], off
	v_lshl_add_u64 v[14:15], v[4:5], 0, s[10:11]
	global_load_dwordx4 v[40:43], v[14:15], off
	v_lshl_add_u64 v[14:15], v[6:7], 0, s[10:11]
	global_load_dwordx4 v[44:47], v[14:15], off
	v_accvgpr_write_b32 a0, 0
	v_accvgpr_write_b32 a1, 0
	v_accvgpr_write_b32 a2, 0
	v_accvgpr_write_b32 a3, 0
	v_accvgpr_write_b32 a4, 0
	v_accvgpr_write_b32 a5, 0
	v_accvgpr_write_b32 a6, 0
	v_accvgpr_write_b32 a7, 0
	v_accvgpr_write_b32 a8, 0
	v_accvgpr_write_b32 a9, 0
	v_accvgpr_write_b32 a10, 0
	v_accvgpr_write_b32 a11, 0
	v_accvgpr_write_b32 a12, 0
	v_accvgpr_write_b32 a13, 0
	v_accvgpr_write_b32 a14, 0
	v_accvgpr_write_b32 a15, 0
	s_waitcnt vmcnt(11)
	ds_write_b128 v13, v[64:67] offset:10240
	s_waitcnt vmcnt(10)
	ds_write_b128 v13, v[68:71] offset:15360
	s_waitcnt vmcnt(9)
	ds_write_b128 v13, v[72:75]
	s_waitcnt vmcnt(8)
	ds_write_b128 v13, v[76:79] offset:5120
	s_waitcnt lgkmcnt(0)
	s_barrier
	v_or_b32_e32 v15, v10, v1
	v_lshlrev_b32_e32 v64, 4, v12
	s_movk_i32 s10, 0x50
	v_or_b32_e32 v14, v11, v1
	v_mul_u32_u24_e32 v65, 0x50, v15
	v_mad_u32_u24 v15, v15, s10, v64
	v_mul_u32_u24_e32 v66, 0x50, v14
	v_mad_u32_u24 v14, v14, s10, v64
	ds_read_b128 v[56:59], v15 offset:15360
	ds_read_b128 v[48:51], v15 offset:10240
	ds_read_b128 v[52:55], v14
	ds_read_b128 v[60:63], v14 offset:5120
	s_nop 7
	v_add_u32_e32 v14, v64, v66
	v_add_u32_e32 v15, v64, v65

.LBB11_9:
	s_endpgm
	s_endpgm
	s_endpgm
	s_endpgm
	s_endpgm
	s_endpgm
	s_endpgm
	s_endpgm
	s_endpgm
	s_endpgm
	s_endpgm
	s_endpgm
	s_endpgm
	s_endpgm
	s_endpgm
	s_endpgm
	s_endpgm
	s_endpgm
	s_endpgm
	s_endpgm
	s_endpgm
	.section	.rodata,"a",@progbits
	.p2align	6, 0x0

.LBB16_4:
	s_load_dwordx4 s[32:35], s[0:1], 0x18
	s_load_dword s36, s[0:1], 0x28
	s_load_dwordx4 s[4:7], s[0:1], 0x60
	s_load_dwordx2 s[14:15], s[0:1], 0x10
	s_ashr_i32 s2, s2, 3
	s_add_i32 s2, s3, s2
	s_abs_i32 s3, s2
	s_waitcnt lgkmcnt(0)
	s_mov_b32 s92, s6
	s_mov_b32 s93, s7
	v_cvt_f32_u32_e32 v100, s6
	v_cvt_f32_u32_e32 v101, s7
	v_cvt_f32_u32_e32 v102, s2
	v_rcp_iflag_f32_e32 v100, v100
	v_rcp_iflag_f32_e32 v101, v101
	v_add_f32_e32 v102, 0.5, v102
	s_nop 0
	v_mul_f32_e32 v102, v102, v100
	v_cvt_u32_f32_e32 v102, v102
	v_cvt_f32_u32_e32 v100, v102
	v_add_f32_e32 v100, 0.5, v100
	v_readfirstlane_b32 s94, v102
	v_mul_f32_e32 v100, v100, v101
	v_cvt_u32_f32_e32 v100, v100
	s_mul_i32 s90, s94, s92
	s_sub_i32 s90, s2, s90
	v_readfirstlane_b32 s95, v100
	s_nop 0
	s_mul_i32 s91, s95, s93
	s_sub_i32 s91, s94, s91
	s_mov_b32 s3, s94
	s_mov_b32 s16, s90
	s_mov_b32 s2, s95
	s_mov_b32 s3, s91
	v_lshrrev_b32_e32 v11, 6, v0
	v_mov_b32_e32 v9, 0
	v_lshlrev_b32_e32 v6, 5, v11
	v_and_b32_e32 v24, 31, v0
	v_and_b32_e32 v25, 63, v0
	v_bfe_u32 v26, v0, 5, 1
	v_lshrrev_b32_e32 v1, 2, v0
	v_lshlrev_b32_e32 v2, 3, v0
	s_mul_i32 s2, s2, s4
	s_lshl_b32 s6, s3, 7
	v_and_b32_e32 v8, 24, v2
	s_ashr_i32 s3, s2, 31
	v_or_b32_e32 v4, s6, v1
	s_ashr_i32 s7, s6, 31
	v_lshl_add_u64 v[2:3], s[2:3], 0, v[8:9]
	s_mul_i32 s17, s14, s7
	v_mad_u64_u32 v[2:3], s[20:21], s14, v4, v[2:3]
	v_mul_lo_u32 v4, s15, v4
	v_lshl_or_b32 v10, s16, 7, v6
	s_lshl_b64 s[18:19], s[14:15], 6
	v_add3_u32 v3, v4, v3, s17
	v_or_b32_e32 v6, v10, v24
	v_lshl_add_u64 v[4:5], v[2:3], 0, s[18:19]
	v_lshlrev_b64 v[2:3], 1, v[2:3]
	v_ashrrev_i32_e32 v7, 31, v6
	v_lshl_add_u64 v[12:13], v[4:5], 1, s[10:11]
	v_lshl_add_u64 v[14:15], s[12:13], 0, v[2:3]
	v_lshl_add_u64 v[16:17], s[10:11], 0, v[2:3]
	s_lshl_b64 s[10:11], s[14:15], 7
	v_lshl_add_u64 v[6:7], v[6:7], 2, s[8:9]
	v_lshl_add_u64 v[18:19], v[14:15], 0, s[10:11]
	global_load_dwordx4 v[126:129], v[16:17], off
	global_load_dwordx4 v[130:133], v[14:15], off
	global_load_dwordx4 v[134:137], v[12:13], off
	global_load_dwordx4 v[138:141], v[18:19], off
	global_load_dword v9, v[6:7], off
	v_lshlrev_b32_e32 v0, 1, v8
	s_movk_i32 s9, 0x50
	s_nop 7
	v_mad_u32_u24 v118, v1, s9, v0
	s_mov_b32 s10, s36
	s_lshr_b32 s3, s3, 28
	s_ashr_i32 s8, s4, 31
	v_lshl_or_b32 v4, s16, 2, v11
	s_add_i32 s2, s2, s3
	s_waitcnt lgkmcnt(0)
	s_ashr_i32 s16, s10, 31
	s_lshr_b32 s8, s8, 27
	s_lshr_b32 s16, s16, 28
	s_ashr_i32 s2, s2, 4
	s_add_i32 s4, s4, s8
	s_add_i32 s10, s10, s16
	s_ashr_i32 s3, s2, 31
	s_ashr_i32 s4, s4, 5
	s_ashr_i32 s10, s10, 4
	v_mov_b32_e32 v2, s2
	v_mov_b32_e32 v3, s3
	s_add_i32 s8, s4, -1
	v_mad_i64_i32 v[2:3], s[2:3], v4, s10, v[2:3]
	s_min_i32 s11, s8, 2
	v_lshlrev_b64 v[2:3], 10, v[2:3]
	v_lshl_or_b32 v2, v25, 4, v2
	s_lshl_b32 s2, s11, 5
	v_lshl_add_u64 v[20:21], s[32:33], 0, v[2:3]
	s_ashr_i32 s3, s2, 31
	global_load_dwordx4 v[46:49], v[16:17], off offset:64
	global_load_dwordx4 v[50:53], v[14:15], off offset:64
	global_load_dwordx4 v[34:37], v[12:13], off offset:64
	global_load_dwordx4 v[30:33], v[18:19], off offset:64
	v_lshl_add_u64 v[22:23], s[34:35], 0, v[2:3]
	global_load_dwordx4 v[66:69], v[20:21], off
	global_load_dwordx4 v[38:41], v[20:21], off offset:1024
	global_load_dwordx4 v[82:85], v[22:23], off
	global_load_dwordx4 v[42:45], v[22:23], off offset:1024
	global_load_dwordx4 v[70:73], v[20:21], off offset:2048
	global_load_dwordx4 v[78:81], v[22:23], off offset:2048
	s_lshl_b64 s[2:3], s[2:3], 1
	v_lshl_add_u64 v[28:29], v[16:17], 0, s[2:3]
	v_lshl_add_u64 v[2:3], v[12:13], 0, s[2:3]
	v_lshl_add_u64 v[4:5], v[14:15], 0, s[2:3]
	v_lshl_add_u64 v[6:7], v[18:19], 0, s[2:3]
	global_load_dwordx4 v[62:65], v[28:29], off
	global_load_dwordx4 v[58:61], v[2:3], off
	global_load_dwordx4 v[74:77], v[4:5], off
	global_load_dwordx4 v[54:57], v[6:7], off
	v_accvgpr_write_b32 a48, 0
	v_accvgpr_write_b32 a49, 0
	v_accvgpr_write_b32 a50, 0
	v_accvgpr_write_b32 a51, 0
	v_accvgpr_write_b32 a52, 0
	v_accvgpr_write_b32 a53, 0
	v_accvgpr_write_b32 a54, 0
	v_accvgpr_write_b32 a55, 0
	v_accvgpr_write_b32 a56, 0
	v_accvgpr_write_b32 a57, 0
	v_accvgpr_write_b32 a58, 0
	v_accvgpr_write_b32 a59, 0
	v_accvgpr_write_b32 a60, 0
	v_accvgpr_write_b32 a61, 0
	v_accvgpr_write_b32 a62, 0
	v_accvgpr_write_b32 a63, 0
	v_accvgpr_write_b32 a32, 0
	v_accvgpr_write_b32 a33, 0
	v_accvgpr_write_b32 a34, 0
	v_accvgpr_write_b32 a35, 0
	v_accvgpr_write_b32 a36, 0
	v_accvgpr_write_b32 a37, 0
	v_accvgpr_write_b32 a38, 0
	v_accvgpr_write_b32 a39, 0
	v_accvgpr_write_b32 a40, 0
	v_accvgpr_write_b32 a41, 0
	v_accvgpr_write_b32 a42, 0
	v_accvgpr_write_b32 a43, 0
	v_accvgpr_write_b32 a44, 0
	v_accvgpr_write_b32 a45, 0
	v_accvgpr_write_b32 a46, 0
	v_accvgpr_write_b32 a47, 0
	v_accvgpr_write_b32 a16, 0
	v_accvgpr_write_b32 a17, 0
	v_accvgpr_write_b32 a18, 0
	v_accvgpr_write_b32 a19, 0
	v_accvgpr_write_b32 a20, 0
	v_accvgpr_write_b32 a21, 0
	v_accvgpr_write_b32 a22, 0
	v_accvgpr_write_b32 a23, 0
	v_accvgpr_write_b32 a24, 0
	v_accvgpr_write_b32 a25, 0
	v_accvgpr_write_b32 a26, 0
	v_accvgpr_write_b32 a27, 0
	v_accvgpr_write_b32 a28, 0
	v_accvgpr_write_b32 a29, 0
	v_accvgpr_write_b32 a30, 0
	v_accvgpr_write_b32 a31, 0
	v_accvgpr_write_b32 a0, 0
	v_accvgpr_write_b32 a1, 0
	v_accvgpr_write_b32 a2, 0
	v_accvgpr_write_b32 a3, 0
	v_accvgpr_write_b32 a4, 0
	v_accvgpr_write_b32 a5, 0
	v_accvgpr_write_b32 a6, 0
	v_accvgpr_write_b32 a7, 0
	v_accvgpr_write_b32 a8, 0
	v_accvgpr_write_b32 a9, 0
	v_accvgpr_write_b32 a10, 0
	v_accvgpr_write_b32 a11, 0
	v_accvgpr_write_b32 a12, 0
	v_accvgpr_write_b32 a13, 0
	v_accvgpr_write_b32 a14, 0
	v_accvgpr_write_b32 a15, 0
	s_waitcnt vmcnt(18)
	ds_write_b128 v118, v[126:129]
	s_waitcnt vmcnt(17)
	ds_write_b128 v118, v[130:133] offset:10240
	s_waitcnt vmcnt(16)
	ds_write_b128 v118, v[134:137] offset:5120
	s_waitcnt vmcnt(15)
	ds_write_b128 v118, v[138:141] offset:15360
	s_waitcnt lgkmcnt(0)
	s_barrier
	v_lshlrev_b32_e32 v2, 4, v26
	v_mad_u32_u24 v4, v24, s9, v2
	ds_read_b128 v[86:89], v4 offset:7680
	ds_read_b128 v[94:97], v4 offset:5120
	ds_read_b128 v[90:93], v4 offset:17920
	ds_read_b128 v[98:101], v4 offset:15360
	ds_read_b128 v[102:105], v4 offset:2560
	ds_read_b128 v[106:109], v4
	ds_read_b128 v[110:113], v4 offset:12800
	ds_read_b128 v[114:117], v4 offset:10240
	v_mul_u32_u24_e32 v1, 0x50, v1
	v_mul_u32_u24_e32 v3, 0x50, v24
	s_mov_b32 s2, 4
	s_nop 7
	v_add_u32_e32 v27, v2, v3
	v_add_u32_e32 v28, v0, v1

.LBB16_7:
	s_load_dwordx4 s[8:11], s[0:1], 0x50
	s_waitcnt vmcnt(4)
	v_mul_u32_u24_e32 v76, 0x2800, v11
	s_load_dword s24, s[0:1], 0x6c
	s_load_dwordx2 s[0:1], s[0:1], 0x40
	v_ashrrev_i32_e32 v11, 31, v10
	v_mov_b32_e32 v0, s6
	v_lshrrev_b32_e32 v4, 2, v25
	v_accvgpr_read_b32 v75, a0
	s_waitcnt lgkmcnt(0)
	s_lshl_b32 s24, s24, 7
	s_mov_b32 s0, 32
	s_mov_b32 s1, 0
	v_mul_lo_u32 v10, v10, s24
	v_mov_b32_e32 v11, 0
	s_mul_i32 s2, s1, s6
	s_mul_i32 s3, s0, s7
	s_add_i32 s4, s3, s2
	v_mad_u64_u32 v[0:1], s[2:3], s0, v0, v[10:11]
	v_or_b32_e32 v0, v0, v8
	v_lshl_or_b32 v77, v8, 1, v76
	v_mul_u32_u24_e32 v8, 40, v4
	s_waitcnt vmcnt(0)
	v_lshl_add_u32 v78, v8, 1, v77
	v_fma_f32 v8, s5, v75, v9
	v_max_f32_e32 v8, 0, v8
	s_mov_b32 s2, 0x43800000
	v_mul_u32_u24_e32 v11, 0xa0, v26
	v_fma_mixlo_f16 v10, v8, s2, 0
	v_or_b32_e32 v11, v11, v24
	v_accvgpr_read_b32 v74, a1
	v_fma_mixlo_f16 v8, v8, s2, -v10 op_sel_hi:[0,0,1]
	v_lshl_or_b32 v26, v11, 1, v76
	s_barrier
	ds_write_b16 v26, v10
	ds_write_b16 v26, v8 offset:5120
	v_fma_f32 v8, s5, v74, v9
	v_max_f32_e32 v8, 0, v8
	v_fma_mixlo_f16 v10, v8, s2, 0
	v_accvgpr_read_b32 v73, a2
	v_fma_mixlo_f16 v8, v8, s2, -v10 op_sel_hi:[0,0,1]
	ds_write_b16 v26, v10 offset:80
	ds_write_b16 v26, v8 offset:5200
	v_fma_f32 v8, s5, v73, v9
	v_max_f32_e32 v8, 0, v8
	v_fma_mixlo_f16 v10, v8, s2, 0
	v_accvgpr_read_b32 v72, a3
	v_fma_mixlo_f16 v8, v8, s2, -v10 op_sel_hi:[0,0,1]
	ds_write_b16 v26, v10 offset:160
	ds_write_b16 v26, v8 offset:5280
	v_fma_f32 v8, s5, v72, v9
	v_max_f32_e32 v8, 0, v8
	v_fma_mixlo_f16 v10, v8, s2, 0
	v_accvgpr_read_b32 v71, a4
	v_fma_mixlo_f16 v8, v8, s2, -v10 op_sel_hi:[0,0,1]
	ds_write_b16 v26, v10 offset:240
	ds_write_b16 v26, v8 offset:5360
	v_fma_f32 v8, s5, v71, v9
	v_max_f32_e32 v8, 0, v8
	v_fma_mixlo_f16 v10, v8, s2, 0
	v_accvgpr_read_b32 v70, a5
	v_fma_mixlo_f16 v8, v8, s2, -v10 op_sel_hi:[0,0,1]
	ds_write_b16 v26, v10 offset:640
	ds_write_b16 v26, v8 offset:5760
	v_fma_f32 v8, s5, v70, v9
	v_max_f32_e32 v8, 0, v8
	v_fma_mixlo_f16 v10, v8, s2, 0
	v_accvgpr_read_b32 v69, a6
	v_fma_mixlo_f16 v8, v8, s2, -v10 op_sel_hi:[0,0,1]
	ds_write_b16 v26, v10 offset:720
	ds_write_b16 v26, v8 offset:5840
	v_fma_f32 v8, s5, v69, v9
	v_max_f32_e32 v8, 0, v8
	v_fma_mixlo_f16 v10, v8, s2, 0
	v_accvgpr_read_b32 v68, a7
	v_fma_mixlo_f16 v8, v8, s2, -v10 op_sel_hi:[0,0,1]
	ds_write_b16 v26, v10 offset:800
	ds_write_b16 v26, v8 offset:5920
	v_fma_f32 v8, s5, v68, v9
	v_max_f32_e32 v8, 0, v8
	v_fma_mixlo_f16 v10, v8, s2, 0
	v_accvgpr_read_b32 v67, a8
	v_fma_mixlo_f16 v8, v8, s2, -v10 op_sel_hi:[0,0,1]
	ds_write_b16 v26, v10 offset:880
	ds_write_b16 v26, v8 offset:6000
	v_fma_f32 v8, s5, v67, v9
	v_max_f32_e32 v8, 0, v8
	v_fma_mixlo_f16 v10, v8, s2, 0
	v_accvgpr_read_b32 v66, a9
	v_fma_mixlo_f16 v8, v8, s2, -v10 op_sel_hi:[0,0,1]
	ds_write_b16 v26, v10 offset:1280
	ds_write_b16 v26, v8 offset:6400
	v_fma_f32 v8, s5, v66, v9
	v_max_f32_e32 v8, 0, v8
	v_fma_mixlo_f16 v10, v8, s2, 0
	v_accvgpr_read_b32 v65, a10
	v_fma_mixlo_f16 v8, v8, s2, -v10 op_sel_hi:[0,0,1]
	ds_write_b16 v26, v10 offset:1360
	ds_write_b16 v26, v8 offset:6480
	v_fma_f32 v8, s5, v65, v9
	v_max_f32_e32 v8, 0, v8
	v_fma_mixlo_f16 v10, v8, s2, 0
	v_accvgpr_read_b32 v64, a11
	v_fma_mixlo_f16 v8, v8, s2, -v10 op_sel_hi:[0,0,1]
	ds_write_b16 v26, v10 offset:1440
	ds_write_b16 v26, v8 offset:6560
	v_fma_f32 v8, s5, v64, v9
	v_max_f32_e32 v8, 0, v8
	v_fma_mixlo_f16 v10, v8, s2, 0
	v_accvgpr_read_b32 v63, a12
	v_fma_mixlo_f16 v8, v8, s2, -v10 op_sel_hi:[0,0,1]
	ds_write_b16 v26, v10 offset:1520
	ds_write_b16 v26, v8 offset:6640
	v_fma_f32 v8, s5, v63, v9
	v_max_f32_e32 v8, 0, v8
	v_fma_mixlo_f16 v10, v8, s2, 0
	v_accvgpr_read_b32 v62, a13
	v_fma_mixlo_f16 v8, v8, s2, -v10 op_sel_hi:[0,0,1]
	ds_write_b16 v26, v10 offset:1920
	ds_write_b16 v26, v8 offset:7040
	v_fma_f32 v8, s5, v62, v9
	v_max_f32_e32 v8, 0, v8
	v_fma_mixlo_f16 v10, v8, s2, 0
	v_accvgpr_read_b32 v61, a14
	v_fma_mixlo_f16 v8, v8, s2, -v10 op_sel_hi:[0,0,1]
	ds_write_b16 v26, v10 offset:2000
	ds_write_b16 v26, v8 offset:7120
	v_fma_f32 v8, s5, v61, v9
	v_max_f32_e32 v8, 0, v8
	v_fma_mixlo_f16 v10, v8, s2, 0
	v_accvgpr_read_b32 v60, a15
	v_fma_mixlo_f16 v8, v8, s2, -v10 op_sel_hi:[0,0,1]
	ds_write_b16 v26, v10 offset:2080
	ds_write_b16 v26, v8 offset:7200
	v_fma_f32 v8, s5, v60, v9
	v_max_f32_e32 v8, 0, v8
	v_fma_mixlo_f16 v10, v8, s2, 0
	v_accvgpr_read_b32 v59, a16
	v_fma_mixlo_f16 v8, v8, s2, -v10 op_sel_hi:[0,0,1]
	ds_write_b16 v26, v10 offset:2160
	ds_write_b16 v26, v8 offset:7280
	v_fma_f32 v8, s5, v59, v9
	v_max_f32_e32 v8, 0, v8
	v_fma_mixlo_f16 v10, v8, s2, 0
	v_accvgpr_read_b32 v58, a17
	v_fma_mixlo_f16 v8, v8, s2, -v10 op_sel_hi:[0,0,1]
	ds_write_b16 v26, v10 offset:2560
	ds_write_b16 v26, v8 offset:7680
	v_fma_f32 v8, s5, v58, v9
	v_max_f32_e32 v8, 0, v8
	v_fma_mixlo_f16 v10, v8, s2, 0
	v_accvgpr_read_b32 v57, a18
	v_fma_mixlo_f16 v8, v8, s2, -v10 op_sel_hi:[0,0,1]
	ds_write_b16 v26, v10 offset:2640
	ds_write_b16 v26, v8 offset:7760
	v_fma_f32 v8, s5, v57, v9
	v_max_f32_e32 v8, 0, v8
	v_fma_mixlo_f16 v10, v8, s2, 0
	v_accvgpr_read_b32 v56, a19
	v_fma_mixlo_f16 v8, v8, s2, -v10 op_sel_hi:[0,0,1]
	ds_write_b16 v26, v10 offset:2720
	ds_write_b16 v26, v8 offset:7840
	v_fma_f32 v8, s5, v56, v9
	v_max_f32_e32 v8, 0, v8
	v_fma_mixlo_f16 v10, v8, s2, 0
	v_accvgpr_read_b32 v55, a20
	v_fma_mixlo_f16 v8, v8, s2, -v10 op_sel_hi:[0,0,1]
	ds_write_b16 v26, v10 offset:2800
	ds_write_b16 v26, v8 offset:7920
	v_fma_f32 v8, s5, v55, v9
	v_max_f32_e32 v8, 0, v8
	v_fma_mixlo_f16 v10, v8, s2, 0
	v_accvgpr_read_b32 v54, a21
	v_fma_mixlo_f16 v8, v8, s2, -v10 op_sel_hi:[0,0,1]
	ds_write_b16 v26, v10 offset:3200
	ds_write_b16 v26, v8 offset:8320
	v_fma_f32 v8, s5, v54, v9
	v_max_f32_e32 v8, 0, v8
	v_fma_mixlo_f16 v10, v8, s2, 0
	v_accvgpr_read_b32 v53, a22
	v_fma_mixlo_f16 v8, v8, s2, -v10 op_sel_hi:[0,0,1]
	ds_write_b16 v26, v10 offset:3280
	ds_write_b16 v26, v8 offset:8400
	v_fma_f32 v8, s5, v53, v9
	v_max_f32_e32 v8, 0, v8
	v_fma_mixlo_f16 v10, v8, s2, 0
	v_accvgpr_read_b32 v52, a23
	v_fma_mixlo_f16 v8, v8, s2, -v10 op_sel_hi:[0,0,1]
	ds_write_b16 v26, v10 offset:3360
	ds_write_b16 v26, v8 offset:8480
	v_fma_f32 v8, s5, v52, v9
	v_max_f32_e32 v8, 0, v8
	v_fma_mixlo_f16 v10, v8, s2, 0
	v_accvgpr_read_b32 v51, a24
	v_fma_mixlo_f16 v8, v8, s2, -v10 op_sel_hi:[0,0,1]
	ds_write_b16 v26, v10 offset:3440
	ds_write_b16 v26, v8 offset:8560
	v_fma_f32 v8, s5, v51, v9
	v_max_f32_e32 v8, 0, v8
	v_fma_mixlo_f16 v10, v8, s2, 0
	v_accvgpr_read_b32 v50, a25
	v_fma_mixlo_f16 v8, v8, s2, -v10 op_sel_hi:[0,0,1]
	ds_write_b16 v26, v10 offset:3840
	ds_write_b16 v26, v8 offset:8960
	v_fma_f32 v8, s5, v50, v9
	v_max_f32_e32 v8, 0, v8
	v_fma_mixlo_f16 v10, v8, s2, 0
	v_accvgpr_read_b32 v49, a26
	v_fma_mixlo_f16 v8, v8, s2, -v10 op_sel_hi:[0,0,1]
	ds_write_b16 v26, v10 offset:3920
	ds_write_b16 v26, v8 offset:9040
	v_fma_f32 v8, s5, v49, v9
	v_max_f32_e32 v8, 0, v8
	v_fma_mixlo_f16 v10, v8, s2, 0
	v_accvgpr_read_b32 v48, a27
	v_fma_mixlo_f16 v8, v8, s2, -v10 op_sel_hi:[0,0,1]
	ds_write_b16 v26, v10 offset:4000
	ds_write_b16 v26, v8 offset:9120
	v_fma_f32 v8, s5, v48, v9
	v_max_f32_e32 v8, 0, v8
	v_fma_mixlo_f16 v10, v8, s2, 0
	v_accvgpr_read_b32 v47, a28
	v_fma_mixlo_f16 v8, v8, s2, -v10 op_sel_hi:[0,0,1]
	ds_write_b16 v26, v10 offset:4080
	ds_write_b16 v26, v8 offset:9200
	v_fma_f32 v8, s5, v47, v9
	v_max_f32_e32 v8, 0, v8
	v_fma_mixlo_f16 v10, v8, s2, 0
	v_accvgpr_read_b32 v46, a29
	v_fma_mixlo_f16 v8, v8, s2, -v10 op_sel_hi:[0,0,1]
	ds_write_b16 v26, v10 offset:4480
	ds_write_b16 v26, v8 offset:9600
	v_fma_f32 v8, s5, v46, v9
	v_max_f32_e32 v8, 0, v8
	v_fma_mixlo_f16 v10, v8, s2, 0
	v_accvgpr_read_b32 v45, a30
	v_fma_mixlo_f16 v8, v8, s2, -v10 op_sel_hi:[0,0,1]
	ds_write_b16 v26, v10 offset:4560
	ds_write_b16 v26, v8 offset:9680
	v_fma_f32 v8, s5, v45, v9
	v_max_f32_e32 v8, 0, v8
	v_fma_mixlo_f16 v10, v8, s2, 0
	v_accvgpr_read_b32 v44, a31
	v_fma_mixlo_f16 v8, v8, s2, -v10 op_sel_hi:[0,0,1]
	ds_write_b16 v26, v10 offset:4640
	ds_write_b16 v26, v8 offset:9760
	v_fma_f32 v8, s5, v44, v9
	v_max_f32_e32 v8, 0, v8
	v_fma_mixlo_f16 v10, v8, s2, 0
	v_fma_mixlo_f16 v8, v8, s2, -v10 op_sel_hi:[0,0,1]
	ds_write_b16 v26, v10 offset:4720
	ds_write_b16 v26, v8 offset:9840
	v_mad_u64_u32 v[10:11], s[6:7], s0, v4, 0
	v_mov_b32_e32 v8, v11
	v_add_u32_e32 v1, s4, v1
	ds_read_b128 v[44:47], v78
	ds_read_b128 v[48:51], v78 offset:5120
	v_mad_u64_u32 v[24:25], s[6:7], s1, v4, v[8:9]
	v_lshlrev_b64 v[0:1], 1, v[0:1]
	v_mov_b32_e32 v11, v24
	v_lshl_add_u64 v[2:3], s[8:9], 0, v[0:1]
	v_lshlrev_b64 v[10:11], 1, v[10:11]
	v_lshl_add_u64 v[0:1], s[10:11], 0, v[0:1]
	v_lshl_add_u64 v[24:25], v[2:3], 0, v[10:11]
	s_waitcnt lgkmcnt(1)
	global_store_dwordx4 v[24:25], v[44:47], off sc1
	v_lshl_add_u64 v[10:11], v[0:1], 0, v[10:11]
	v_or_b32_e32 v24, 16, v4
	s_waitcnt lgkmcnt(0)
	global_store_dwordx4 v[10:11], v[48:51], off sc1
	v_mul_u32_u24_e32 v8, 40, v24
	v_mad_u64_u32 v[10:11], s[6:7], s0, v24, 0
	v_lshl_add_u32 v56, v8, 1, v77
	v_mov_b32_e32 v8, v11
	ds_read_b128 v[44:47], v56
	ds_read_b128 v[48:51], v56 offset:5120
	v_mad_u64_u32 v[24:25], s[6:7], s1, v24, v[8:9]
	v_mov_b32_e32 v11, v24
	v_lshlrev_b64 v[10:11], 1, v[10:11]
	v_lshl_add_u64 v[24:25], v[2:3], 0, v[10:11]
	s_waitcnt lgkmcnt(1)
	global_store_dwordx4 v[24:25], v[44:47], off sc1
	v_lshl_add_u64 v[10:11], v[0:1], 0, v[10:11]
	v_or_b32_e32 v24, 32, v4
	s_waitcnt lgkmcnt(0)
	global_store_dwordx4 v[10:11], v[48:51], off sc1
	v_mad_u64_u32 v[10:11], s[6:7], s0, v24, 0
	ds_read_b128 v[52:55], v56 offset:1280
	ds_read_b128 v[44:47], v56 offset:2560
	v_mov_b32_e32 v8, v11
	ds_read_b128 v[48:51], v56 offset:6400
	v_mad_u64_u32 v[24:25], s[6:7], s1, v24, v[8:9]
	v_mov_b32_e32 v11, v24
	v_lshlrev_b64 v[10:11], 1, v[10:11]
	v_lshl_add_u64 v[24:25], v[2:3], 0, v[10:11]
	s_waitcnt lgkmcnt(2)
	global_store_dwordx4 v[24:25], v[52:55], off sc1
	v_lshl_add_u64 v[10:11], v[0:1], 0, v[10:11]
	v_or_b32_e32 v24, 48, v4
	ds_read_b128 v[52:55], v56 offset:7680
	s_waitcnt lgkmcnt(1)
	global_store_dwordx4 v[10:11], v[48:51], off sc1
	v_mad_u64_u32 v[10:11], s[6:7], s0, v24, 0
	v_mov_b32_e32 v8, v11
	v_mad_u64_u32 v[24:25], s[6:7], s1, v24, v[8:9]
	v_accvgpr_read_b32 v43, a32
	v_mov_b32_e32 v11, v24
	v_lshlrev_b64 v[10:11], 1, v[10:11]
	v_fma_f32 v8, s5, v43, v9
	v_lshl_add_u64 v[24:25], v[2:3], 0, v[10:11]
	v_lshl_add_u64 v[10:11], v[0:1], 0, v[10:11]
	v_max_f32_e32 v8, 0, v8
	s_waitcnt lgkmcnt(0)
	global_store_dwordx4 v[10:11], v[52:55], off sc1
	v_fma_mixlo_f16 v10, v8, s2, 0
	v_accvgpr_read_b32 v42, a33
	v_fma_mixlo_f16 v8, v8, s2, -v10 op_sel_hi:[0,0,1]
	global_store_dwordx4 v[24:25], v[44:47], off sc1
	ds_write_b16 v26, v10
	ds_write_b16 v26, v8 offset:5120
	v_fma_f32 v8, s5, v42, v9
	v_max_f32_e32 v8, 0, v8
	v_fma_mixlo_f16 v10, v8, s2, 0
	v_accvgpr_read_b32 v41, a34
	v_fma_mixlo_f16 v8, v8, s2, -v10 op_sel_hi:[0,0,1]
	ds_write_b16 v26, v10 offset:80
	ds_write_b16 v26, v8 offset:5200
	v_fma_f32 v8, s5, v41, v9
	v_max_f32_e32 v8, 0, v8
	v_fma_mixlo_f16 v10, v8, s2, 0
	v_accvgpr_read_b32 v40, a35
	v_fma_mixlo_f16 v8, v8, s2, -v10 op_sel_hi:[0,0,1]
	ds_write_b16 v26, v10 offset:160
	ds_write_b16 v26, v8 offset:5280
	v_fma_f32 v8, s5, v40, v9
	v_max_f32_e32 v8, 0, v8
	v_fma_mixlo_f16 v10, v8, s2, 0
	v_accvgpr_read_b32 v39, a36
	v_fma_mixlo_f16 v8, v8, s2, -v10 op_sel_hi:[0,0,1]
	ds_write_b16 v26, v10 offset:240
	ds_write_b16 v26, v8 offset:5360
	v_fma_f32 v8, s5, v39, v9
	v_max_f32_e32 v8, 0, v8
	v_fma_mixlo_f16 v10, v8, s2, 0
	v_accvgpr_read_b32 v38, a37
	v_fma_mixlo_f16 v8, v8, s2, -v10 op_sel_hi:[0,0,1]
	ds_write_b16 v26, v10 offset:640
	ds_write_b16 v26, v8 offset:5760
	v_fma_f32 v8, s5, v38, v9
	v_max_f32_e32 v8, 0, v8
	v_fma_mixlo_f16 v10, v8, s2, 0
	v_accvgpr_read_b32 v37, a38
	v_fma_mixlo_f16 v8, v8, s2, -v10 op_sel_hi:[0,0,1]
	ds_write_b16 v26, v10 offset:720
	ds_write_b16 v26, v8 offset:5840
	v_fma_f32 v8, s5, v37, v9
	v_max_f32_e32 v8, 0, v8
	v_fma_mixlo_f16 v10, v8, s2, 0
	v_accvgpr_read_b32 v36, a39
	v_fma_mixlo_f16 v8, v8, s2, -v10 op_sel_hi:[0,0,1]
	ds_write_b16 v26, v10 offset:800
	ds_write_b16 v26, v8 offset:5920
	v_fma_f32 v8, s5, v36, v9
	v_max_f32_e32 v8, 0, v8
	v_fma_mixlo_f16 v10, v8, s2, 0
	v_accvgpr_read_b32 v35, a40
	v_fma_mixlo_f16 v8, v8, s2, -v10 op_sel_hi:[0,0,1]
	ds_write_b16 v26, v10 offset:880
	ds_write_b16 v26, v8 offset:6000
	v_fma_f32 v8, s5, v35, v9
	v_max_f32_e32 v8, 0, v8
	v_fma_mixlo_f16 v10, v8, s2, 0
	v_accvgpr_read_b32 v34, a41
	v_fma_mixlo_f16 v8, v8, s2, -v10 op_sel_hi:[0,0,1]
	ds_write_b16 v26, v10 offset:1280
	ds_write_b16 v26, v8 offset:6400
	v_fma_f32 v8, s5, v34, v9
	v_max_f32_e32 v8, 0, v8
	v_fma_mixlo_f16 v10, v8, s2, 0
	v_accvgpr_read_b32 v33, a42
	v_fma_mixlo_f16 v8, v8, s2, -v10 op_sel_hi:[0,0,1]
	ds_write_b16 v26, v10 offset:1360
	ds_write_b16 v26, v8 offset:6480
	v_fma_f32 v8, s5, v33, v9
	v_max_f32_e32 v8, 0, v8
	v_fma_mixlo_f16 v10, v8, s2, 0
	v_accvgpr_read_b32 v32, a43
	v_fma_mixlo_f16 v8, v8, s2, -v10 op_sel_hi:[0,0,1]
	ds_write_b16 v26, v10 offset:1440
	ds_write_b16 v26, v8 offset:6560
	v_fma_f32 v8, s5, v32, v9
	v_max_f32_e32 v8, 0, v8
	v_fma_mixlo_f16 v10, v8, s2, 0
	v_accvgpr_read_b32 v31, a44
	v_fma_mixlo_f16 v8, v8, s2, -v10 op_sel_hi:[0,0,1]
	ds_write_b16 v26, v10 offset:1520
	ds_write_b16 v26, v8 offset:6640
	v_fma_f32 v8, s5, v31, v9
	v_max_f32_e32 v8, 0, v8
	v_fma_mixlo_f16 v10, v8, s2, 0
	v_accvgpr_read_b32 v30, a45
	v_fma_mixlo_f16 v8, v8, s2, -v10 op_sel_hi:[0,0,1]
	ds_write_b16 v26, v10 offset:1920
	ds_write_b16 v26, v8 offset:7040
	v_fma_f32 v8, s5, v30, v9
	v_max_f32_e32 v8, 0, v8
	v_fma_mixlo_f16 v10, v8, s2, 0
	v_accvgpr_read_b32 v29, a46
	v_fma_mixlo_f16 v8, v8, s2, -v10 op_sel_hi:[0,0,1]
	ds_write_b16 v26, v10 offset:2000
	ds_write_b16 v26, v8 offset:7120
	v_fma_f32 v8, s5, v29, v9
	v_max_f32_e32 v8, 0, v8
	v_fma_mixlo_f16 v10, v8, s2, 0
	v_accvgpr_read_b32 v28, a47
	v_fma_mixlo_f16 v8, v8, s2, -v10 op_sel_hi:[0,0,1]
	ds_write_b16 v26, v10 offset:2080
	ds_write_b16 v26, v8 offset:7200
	v_fma_f32 v8, s5, v28, v9
	v_max_f32_e32 v8, 0, v8
	v_fma_mixlo_f16 v10, v8, s2, 0
	v_accvgpr_read_b32 v27, a48
	v_fma_mixlo_f16 v8, v8, s2, -v10 op_sel_hi:[0,0,1]
	ds_write_b16 v26, v10 offset:2160
	ds_write_b16 v26, v8 offset:7280
	v_fma_f32 v8, s5, v27, v9
	v_max_f32_e32 v8, 0, v8
	v_fma_mixlo_f16 v10, v8, s2, 0
	v_accvgpr_read_b32 v23, a49
	v_fma_mixlo_f16 v8, v8, s2, -v10 op_sel_hi:[0,0,1]
	ds_write_b16 v26, v10 offset:2560
	ds_write_b16 v26, v8 offset:7680
	v_fma_f32 v8, s5, v23, v9
	v_max_f32_e32 v8, 0, v8
	v_fma_mixlo_f16 v10, v8, s2, 0
	v_accvgpr_read_b32 v22, a50
	v_fma_mixlo_f16 v8, v8, s2, -v10 op_sel_hi:[0,0,1]
	ds_write_b16 v26, v10 offset:2640
	ds_write_b16 v26, v8 offset:7760
	v_fma_f32 v8, s5, v22, v9
	v_max_f32_e32 v8, 0, v8
	v_fma_mixlo_f16 v10, v8, s2, 0
	v_accvgpr_read_b32 v21, a51
	v_fma_mixlo_f16 v8, v8, s2, -v10 op_sel_hi:[0,0,1]
	ds_write_b16 v26, v10 offset:2720
	ds_write_b16 v26, v8 offset:7840
	v_fma_f32 v8, s5, v21, v9
	v_max_f32_e32 v8, 0, v8
	v_fma_mixlo_f16 v10, v8, s2, 0
	v_accvgpr_read_b32 v20, a52
	v_fma_mixlo_f16 v8, v8, s2, -v10 op_sel_hi:[0,0,1]
	ds_write_b16 v26, v10 offset:2800
	ds_write_b16 v26, v8 offset:7920
	v_fma_f32 v8, s5, v20, v9
	v_max_f32_e32 v8, 0, v8
	v_fma_mixlo_f16 v10, v8, s2, 0
	v_accvgpr_read_b32 v19, a53
	v_fma_mixlo_f16 v8, v8, s2, -v10 op_sel_hi:[0,0,1]
	ds_write_b16 v26, v10 offset:3200
	ds_write_b16 v26, v8 offset:8320
	v_fma_f32 v8, s5, v19, v9
	v_max_f32_e32 v8, 0, v8
	v_fma_mixlo_f16 v10, v8, s2, 0
	v_accvgpr_read_b32 v18, a54
	v_fma_mixlo_f16 v8, v8, s2, -v10 op_sel_hi:[0,0,1]
	ds_write_b16 v26, v10 offset:3280
	ds_write_b16 v26, v8 offset:8400
	v_fma_f32 v8, s5, v18, v9
	v_max_f32_e32 v8, 0, v8
	v_fma_mixlo_f16 v10, v8, s2, 0
	v_accvgpr_read_b32 v17, a55
	v_fma_mixlo_f16 v8, v8, s2, -v10 op_sel_hi:[0,0,1]
	ds_write_b16 v26, v10 offset:3360
	ds_write_b16 v26, v8 offset:8480
	v_fma_f32 v8, s5, v17, v9
	v_max_f32_e32 v8, 0, v8
	v_fma_mixlo_f16 v10, v8, s2, 0
	v_accvgpr_read_b32 v16, a56
	v_fma_mixlo_f16 v8, v8, s2, -v10 op_sel_hi:[0,0,1]
	ds_write_b16 v26, v10 offset:3440
	ds_write_b16 v26, v8 offset:8560
	v_fma_f32 v8, s5, v16, v9
	v_max_f32_e32 v8, 0, v8
	v_fma_mixlo_f16 v10, v8, s2, 0
	v_accvgpr_read_b32 v15, a57
	v_fma_mixlo_f16 v8, v8, s2, -v10 op_sel_hi:[0,0,1]
	ds_write_b16 v26, v10 offset:3840
	ds_write_b16 v26, v8 offset:8960
	v_fma_f32 v8, s5, v15, v9
	v_max_f32_e32 v8, 0, v8
	v_fma_mixlo_f16 v10, v8, s2, 0
	v_accvgpr_read_b32 v14, a58
	v_fma_mixlo_f16 v8, v8, s2, -v10 op_sel_hi:[0,0,1]
	ds_write_b16 v26, v10 offset:3920
	ds_write_b16 v26, v8 offset:9040
	v_fma_f32 v8, s5, v14, v9
	v_max_f32_e32 v8, 0, v8
	v_fma_mixlo_f16 v10, v8, s2, 0
	v_accvgpr_read_b32 v13, a59
	v_fma_mixlo_f16 v8, v8, s2, -v10 op_sel_hi:[0,0,1]
	ds_write_b16 v26, v10 offset:4000
	ds_write_b16 v26, v8 offset:9120
	v_fma_f32 v8, s5, v13, v9
	v_max_f32_e32 v8, 0, v8
	v_fma_mixlo_f16 v10, v8, s2, 0
	v_accvgpr_read_b32 v12, a60
	v_fma_mixlo_f16 v8, v8, s2, -v10 op_sel_hi:[0,0,1]
	ds_write_b16 v26, v10 offset:4080
	ds_write_b16 v26, v8 offset:9200
	v_fma_f32 v8, s5, v12, v9
	v_accvgpr_read_b32 v7, a61
	v_max_f32_e32 v8, 0, v8
	v_fma_mixlo_f16 v10, v8, s2, 0
	v_fma_f32 v7, s5, v7, v9
	v_accvgpr_read_b32 v6, a62
	v_fma_mixlo_f16 v8, v8, s2, -v10 op_sel_hi:[0,0,1]
	v_max_f32_e32 v7, 0, v7
	ds_write_b16 v26, v10 offset:4480
	ds_write_b16 v26, v8 offset:9600
	v_fma_mixlo_f16 v8, v7, s2, 0
	v_fma_f32 v6, s5, v6, v9
	v_accvgpr_read_b32 v5, a63
	v_fma_mixlo_f16 v7, v7, s2, -v8 op_sel_hi:[0,0,1]
	v_max_f32_e32 v6, 0, v6
	ds_write_b16 v26, v8 offset:4560
	ds_write_b16 v26, v7 offset:9680
	v_fma_mixlo_f16 v7, v6, s2, 0
	v_fmac_f32_e32 v9, s5, v5
	v_fma_mixlo_f16 v6, v6, s2, -v7 op_sel_hi:[0,0,1]
	v_max_f32_e32 v5, 0, v9
	ds_write_b16 v26, v7 offset:4640
	ds_write_b16 v26, v6 offset:9760
	v_fma_mixlo_f16 v6, v5, s2, 0
	v_fma_mixlo_f16 v5, v5, s2, -v6 op_sel_hi:[0,0,1]
	ds_write_b16 v26, v6 offset:4720
	ds_write_b16 v26, v5 offset:9840
	v_or_b32_e32 v5, 64, v4
	v_mad_u64_u32 v[14:15], s[2:3], s0, v5, 0
	v_mov_b32_e32 v16, v15
	ds_read_b128 v[6:9], v78
	ds_read_b128 v[10:13], v78 offset:5120
	v_mad_u64_u32 v[16:17], s[2:3], s1, v5, v[16:17]
	v_mov_b32_e32 v15, v16
	v_lshlrev_b64 v[14:15], 1, v[14:15]
	v_lshl_add_u64 v[16:17], v[2:3], 0, v[14:15]
	s_waitcnt lgkmcnt(1)
	global_store_dwordx4 v[16:17], v[6:9], off sc1
	v_or_b32_e32 v5, 0x50, v4
	s_nop 0
	v_lshl_add_u64 v[6:7], v[0:1], 0, v[14:15]
	s_waitcnt lgkmcnt(0)
	global_store_dwordx4 v[6:7], v[10:13], off sc1
	v_mad_u64_u32 v[14:15], s[2:3], s0, v5, 0
	ds_read_b128 v[6:9], v56
	ds_read_b128 v[10:13], v56 offset:5120
	v_mov_b32_e32 v16, v15
	v_mad_u64_u32 v[16:17], s[2:3], s1, v5, v[16:17]
	v_mov_b32_e32 v15, v16
	v_lshlrev_b64 v[18:19], 1, v[14:15]
	v_lshl_add_u64 v[20:21], v[2:3], 0, v[18:19]
	v_lshl_add_u64 v[18:19], v[0:1], 0, v[18:19]
	v_or_b32_e32 v5, 0x60, v4
	s_waitcnt lgkmcnt(0)
	global_store_dwordx4 v[18:19], v[10:13], off sc1
	v_mad_u64_u32 v[18:19], s[2:3], s0, v5, 0
	ds_read_b128 v[14:17], v56 offset:1280
	global_store_dwordx4 v[20:21], v[6:9], off sc1
	ds_read_b128 v[10:13], v56 offset:6400
	v_mov_b32_e32 v20, v19
	v_mad_u64_u32 v[20:21], s[2:3], s1, v5, v[20:21]
	v_mov_b32_e32 v19, v20
	v_lshlrev_b64 v[18:19], 1, v[18:19]
	v_lshl_add_u64 v[20:21], v[2:3], 0, v[18:19]
	v_lshl_add_u64 v[18:19], v[0:1], 0, v[18:19]
	ds_read_b128 v[6:9], v56 offset:2560
	s_waitcnt lgkmcnt(2)
	global_store_dwordx4 v[20:21], v[14:17], off sc1
	ds_read_b128 v[14:17], v56 offset:7680
	s_waitcnt lgkmcnt(2)
	global_store_dwordx4 v[18:19], v[10:13], off sc1
	s_nop 1
	v_or_b32_e32 v11, 0x70, v4
	v_mad_u64_u32 v[4:5], s[2:3], s0, v11, 0
	v_mov_b32_e32 v10, v5
	v_mad_u64_u32 v[10:11], s[0:1], s1, v11, v[10:11]
	v_mov_b32_e32 v5, v10
	v_lshlrev_b64 v[4:5], 1, v[4:5]
	v_lshl_add_u64 v[2:3], v[2:3], 0, v[4:5]
	v_lshl_add_u64 v[0:1], v[0:1], 0, v[4:5]
	s_waitcnt lgkmcnt(1)
	global_store_dwordx4 v[2:3], v[6:9], off sc1
	s_waitcnt lgkmcnt(0)
	global_store_dwordx4 v[0:1], v[14:17], off sc1
	s_endpgm
	s_endpgm
	s_endpgm
	s_endpgm
	s_endpgm
	s_endpgm
	s_endpgm
	s_endpgm
	s_endpgm
	s_endpgm
	.section	.rodata,"a",@progbits
	.p2align	6, 0x0

.LBB17_4:
	s_load_dwordx4 s[4:7], s[0:1], 0x60
	s_load_dwordx2 s[14:15], s[0:1], 0x10
	s_ashr_i32 s2, s2, 3
	s_add_i32 s2, s3, s2
	s_abs_i32 s3, s2
	s_waitcnt lgkmcnt(0)
	s_mov_b32 s92, s6
	s_mov_b32 s93, s7
	v_cvt_f32_u32_e32 v72, s6
	v_cvt_f32_u32_e32 v73, s7
	v_cvt_f32_u32_e32 v74, s2
	v_rcp_iflag_f32_e32 v72, v72
	v_rcp_iflag_f32_e32 v73, v73
	v_add_f32_e32 v74, 0.5, v74
	s_nop 0
	v_mul_f32_e32 v74, v74, v72
	v_cvt_u32_f32_e32 v74, v74
	v_cvt_f32_u32_e32 v72, v74
	v_add_f32_e32 v72, 0.5, v72
	v_readfirstlane_b32 s94, v74
	v_mul_f32_e32 v72, v72, v73
	v_cvt_u32_f32_e32 v72, v72
	s_mul_i32 s90, s94, s92
	s_sub_i32 s90, s2, s90
	v_readfirstlane_b32 s95, v72
	s_nop 0
	s_mul_i32 s91, s95, s93
	s_sub_i32 s91, s94, s91
	s_mov_b32 s3, s94
	s_mov_b32 s16, s90
	s_mov_b32 s2, s95
	s_mov_b32 s3, s91
	v_lshrrev_b32_e32 v5, 6, v0
	v_lshrrev_b32_e32 v15, 2, v0
	v_mov_b32_e32 v3, 0
	v_and_b32_e32 v13, 31, v0
	v_lshlrev_b32_e32 v1, 3, v0
	s_mul_i32 s2, s2, s4
	s_lshl_b32 s6, s3, 6
	v_and_b32_e32 v2, 24, v1
	s_ashr_i32 s3, s2, 31
	v_or_b32_e32 v1, s6, v15
	s_ashr_i32 s7, s6, 31
	v_lshl_add_u64 v[6:7], s[2:3], 0, v[2:3]
	v_lshlrev_b32_e32 v3, 5, v5
	v_lshl_or_b32 v4, s16, 7, v3
	s_mul_i32 s17, s14, s7
	v_mad_u64_u32 v[6:7], s[18:19], s14, v1, v[6:7]
	v_mul_lo_u32 v1, s15, v1
	v_add3_u32 v7, v1, v7, s17
	v_or_b32_e32 v10, v4, v13
	v_lshlrev_b64 v[8:9], 1, v[6:7]
	v_ashrrev_i32_e32 v11, 31, v10
	v_lshl_add_u64 v[6:7], s[10:11], 0, v[8:9]
	v_lshl_add_u64 v[8:9], s[8:9], 0, v[8:9]
	v_lshl_add_u64 v[10:11], v[10:11], 2, s[12:13]
	global_load_dwordx4 v[18:21], v[8:9], off
	global_load_dwordx4 v[22:25], v[6:7], off
	global_load_dword v12, v[10:11], off
	s_movk_i32 s9, 0x50
	v_lshlrev_b32_e32 v16, 1, v2
	v_and_b32_e32 v3, 63, v0
	s_nop 7
	v_bfe_u32 v14, v0, 5, 1
	v_mad_u32_u24 v0, v15, s9, v16
	s_cmp_lt_i32 s4, 32
	v_accvgpr_write_b32 a0, 0
	v_accvgpr_write_b32 a1, 0
	v_accvgpr_write_b32 a2, 0
	v_accvgpr_write_b32 a3, 0
	v_accvgpr_write_b32 a4, 0
	v_accvgpr_write_b32 a5, 0
	v_accvgpr_write_b32 a6, 0
	v_accvgpr_write_b32 a7, 0
	v_accvgpr_write_b32 a8, 0
	v_accvgpr_write_b32 a9, 0
	v_accvgpr_write_b32 a10, 0
	v_accvgpr_write_b32 a11, 0
	v_accvgpr_write_b32 a12, 0
	v_accvgpr_write_b32 a13, 0
	v_accvgpr_write_b32 a14, 0
	v_accvgpr_write_b32 a15, 0
	v_accvgpr_write_b32 a16, 0
	v_accvgpr_write_b32 a17, 0
	v_accvgpr_write_b32 a18, 0
	v_accvgpr_write_b32 a19, 0
	v_accvgpr_write_b32 a20, 0
	v_accvgpr_write_b32 a21, 0
	v_accvgpr_write_b32 a22, 0
	v_accvgpr_write_b32 a23, 0
	v_accvgpr_write_b32 a24, 0
	v_accvgpr_write_b32 a25, 0
	v_accvgpr_write_b32 a26, 0
	v_accvgpr_write_b32 a27, 0
	v_accvgpr_write_b32 a28, 0
	v_accvgpr_write_b32 a29, 0
	v_accvgpr_write_b32 a30, 0
	v_accvgpr_write_b32 a31, 0
	s_waitcnt vmcnt(2)
	ds_write_b128 v0, v[18:21]
	s_waitcnt vmcnt(1)
	ds_write_b128 v0, v[22:25] offset:5120
	s_waitcnt lgkmcnt(0)
	s_barrier
	s_cbranch_scc1 .LBB17_7
	s_load_dwordx4 s[12:15], s[0:1], 0x18
	s_load_dword s10, s[0:1], 0x28
	s_lshr_b32 s3, s3, 28
	v_lshl_or_b32 v10, s16, 2, v5
	s_add_i32 s2, s2, s3
	s_ashr_i32 s2, s2, 4
	s_waitcnt lgkmcnt(0)
	s_ashr_i32 s16, s10, 31
	s_lshr_b32 s16, s16, 28
	s_ashr_i32 s8, s4, 31
	s_add_i32 s10, s10, s16
	s_ashr_i32 s3, s2, 31
	s_lshr_b32 s8, s8, 27
	s_ashr_i32 s10, s10, 4
	v_mov_b32_e32 v0, s2
	v_mov_b32_e32 v1, s3
	s_add_i32 s4, s4, s8
	v_mad_i64_i32 v[0:1], s[2:3], v10, s10, v[0:1]
	s_ashr_i32 s4, s4, 5
	v_lshlrev_b64 v[10:11], 10, v[0:1]
	s_add_i32 s8, s4, -1
	v_lshl_or_b32 v10, v3, 4, v10
	s_min_i32 s11, s8, 2
	v_lshl_add_u64 v[0:1], s[12:13], 0, v[10:11]
	global_load_dwordx4 v[30:33], v[8:9], off offset:64
	global_load_dwordx4 v[22:25], v[6:7], off offset:64
	v_lshl_add_u64 v[10:11], s[14:15], 0, v[10:11]
	global_load_dwordx4 v[38:41], v[0:1], off
	global_load_dwordx4 v[18:21], v[0:1], off offset:1024
	global_load_dwordx4 v[54:57], v[10:11], off
	global_load_dwordx4 v[26:29], v[10:11], off offset:1024
	global_load_dwordx4 v[42:45], v[0:1], off offset:2048
	global_load_dwordx4 v[50:53], v[10:11], off offset:2048
	s_lshl_b32 s2, s11, 5
	s_ashr_i32 s3, s2, 31
	s_lshl_b64 s[2:3], s[2:3], 1
	v_lshl_add_u64 v[60:61], v[8:9], 0, s[2:3]
	v_lshl_add_u64 v[58:59], v[6:7], 0, s[2:3]
	global_load_dwordx4 v[46:49], v[60:61], off
	global_load_dwordx4 v[34:37], v[58:59], off
	v_mul_u32_u24_e32 v17, 0x50, v15
	v_lshlrev_b32_e32 v15, 4, v14
	v_mad_u32_u24 v70, v13, s9, v15
	ds_read_b128 v[58:61], v70 offset:2560
	ds_read_b128 v[66:69], v70
	ds_read_b128 v[62:65], v70 offset:7680
	ds_read_b128 v[70:73], v70 offset:5120
	v_mul_u32_u24_e32 v74, 0x50, v13
	s_mov_b32 s2, 4
	s_nop 7
	v_add_u32_e32 v15, v15, v74
	v_add_u32_e32 v16, v16, v17

.LBB17_7:
	s_load_dwordx4 s[8:11], s[0:1], 0x50
	s_waitcnt vmcnt(7)
	v_accvgpr_read_b32 v39, a1
	s_load_dwordx2 s[0:1], s[0:1], 0x40
	v_mul_u32_u24_e32 v41, 0x2800, v5
	v_ashrrev_i32_e32 v5, 31, v4
	v_mov_b32_e32 v0, s6
	v_mul_u32_u24_e32 v14, 0xa0, v14
	s_waitcnt lgkmcnt(0)
	s_mul_i32 s2, s1, s6
	s_mul_i32 s3, s0, s7
	v_accvgpr_read_b32 v40, a0
	s_add_i32 s4, s3, s2
	v_mad_u64_u32 v[0:1], s[2:3], s0, v0, v[4:5]
	v_or_b32_e32 v13, v14, v13
	s_waitcnt vmcnt(0)
	v_fma_f32 v14, s5, v39, v12
	v_fma_f32 v40, s5, v40, v12
	s_mov_b32 s2, 0x43800000
	v_max_f32_e32 v14, 0, v14
	v_max_f32_e32 v40, 0, v40
	v_fma_mixlo_f16 v39, v14, s2, 0
	v_accvgpr_read_b32 v38, a2
	v_fma_mixlo_f16 v42, v40, s2, 0
	v_lshl_or_b32 v13, v13, 1, v41
	v_fma_mixlo_f16 v14, v14, s2, -v39 op_sel_hi:[0,0,1]
	s_barrier
	v_fma_mixlo_f16 v40, v40, s2, -v42 op_sel_hi:[0,0,1]
	ds_write_b16 v13, v42
	ds_write_b16 v13, v40 offset:5120
	ds_write_b16 v13, v39 offset:80
	ds_write_b16 v13, v14 offset:5200
	v_fma_f32 v14, s5, v38, v12
	v_max_f32_e32 v14, 0, v14
	v_fma_mixlo_f16 v38, v14, s2, 0
	v_accvgpr_read_b32 v37, a3
	v_fma_mixlo_f16 v14, v14, s2, -v38 op_sel_hi:[0,0,1]
	ds_write_b16 v13, v38 offset:160
	ds_write_b16 v13, v14 offset:5280
	v_fma_f32 v14, s5, v37, v12
	v_max_f32_e32 v14, 0, v14
	v_fma_mixlo_f16 v37, v14, s2, 0
	v_accvgpr_read_b32 v36, a4
	v_fma_mixlo_f16 v14, v14, s2, -v37 op_sel_hi:[0,0,1]
	ds_write_b16 v13, v37 offset:240
	ds_write_b16 v13, v14 offset:5360
	v_fma_f32 v14, s5, v36, v12
	v_max_f32_e32 v14, 0, v14
	v_fma_mixlo_f16 v36, v14, s2, 0
	v_accvgpr_read_b32 v35, a5
	v_fma_mixlo_f16 v14, v14, s2, -v36 op_sel_hi:[0,0,1]
	ds_write_b16 v13, v36 offset:640
	ds_write_b16 v13, v14 offset:5760
	v_fma_f32 v14, s5, v35, v12
	v_max_f32_e32 v14, 0, v14
	v_fma_mixlo_f16 v35, v14, s2, 0
	v_accvgpr_read_b32 v34, a6
	v_fma_mixlo_f16 v14, v14, s2, -v35 op_sel_hi:[0,0,1]
	ds_write_b16 v13, v35 offset:720
	ds_write_b16 v13, v14 offset:5840
	v_fma_f32 v14, s5, v34, v12
	v_max_f32_e32 v14, 0, v14
	v_fma_mixlo_f16 v34, v14, s2, 0
	v_accvgpr_read_b32 v33, a7
	v_fma_mixlo_f16 v14, v14, s2, -v34 op_sel_hi:[0,0,1]
	ds_write_b16 v13, v34 offset:800
	ds_write_b16 v13, v14 offset:5920
	v_fma_f32 v14, s5, v33, v12
	v_max_f32_e32 v14, 0, v14
	v_fma_mixlo_f16 v33, v14, s2, 0
	v_accvgpr_read_b32 v32, a8
	v_fma_mixlo_f16 v14, v14, s2, -v33 op_sel_hi:[0,0,1]
	ds_write_b16 v13, v33 offset:880
	ds_write_b16 v13, v14 offset:6000
	v_fma_f32 v14, s5, v32, v12
	v_max_f32_e32 v14, 0, v14
	v_fma_mixlo_f16 v32, v14, s2, 0
	v_accvgpr_read_b32 v31, a9
	v_fma_mixlo_f16 v14, v14, s2, -v32 op_sel_hi:[0,0,1]
	ds_write_b16 v13, v32 offset:1280
	ds_write_b16 v13, v14 offset:6400
	v_fma_f32 v14, s5, v31, v12
	v_max_f32_e32 v14, 0, v14
	v_fma_mixlo_f16 v31, v14, s2, 0
	v_accvgpr_read_b32 v30, a10
	v_fma_mixlo_f16 v14, v14, s2, -v31 op_sel_hi:[0,0,1]
	ds_write_b16 v13, v31 offset:1360
	ds_write_b16 v13, v14 offset:6480
	v_fma_f32 v14, s5, v30, v12
	v_max_f32_e32 v14, 0, v14
	v_fma_mixlo_f16 v30, v14, s2, 0
	v_accvgpr_read_b32 v29, a11
	v_fma_mixlo_f16 v14, v14, s2, -v30 op_sel_hi:[0,0,1]
	ds_write_b16 v13, v30 offset:1440
	ds_write_b16 v13, v14 offset:6560
	v_fma_f32 v14, s5, v29, v12
	v_max_f32_e32 v14, 0, v14
	v_fma_mixlo_f16 v29, v14, s2, 0
	v_accvgpr_read_b32 v28, a12
	v_fma_mixlo_f16 v14, v14, s2, -v29 op_sel_hi:[0,0,1]
	ds_write_b16 v13, v29 offset:1520
	ds_write_b16 v13, v14 offset:6640
	v_fma_f32 v14, s5, v28, v12
	v_max_f32_e32 v14, 0, v14
	v_fma_mixlo_f16 v28, v14, s2, 0
	v_accvgpr_read_b32 v27, a13
	v_fma_mixlo_f16 v14, v14, s2, -v28 op_sel_hi:[0,0,1]
	ds_write_b16 v13, v28 offset:1920
	ds_write_b16 v13, v14 offset:7040
	v_fma_f32 v14, s5, v27, v12
	v_max_f32_e32 v14, 0, v14
	v_fma_mixlo_f16 v27, v14, s2, 0
	v_accvgpr_read_b32 v26, a14
	v_fma_mixlo_f16 v14, v14, s2, -v27 op_sel_hi:[0,0,1]
	ds_write_b16 v13, v27 offset:2000
	ds_write_b16 v13, v14 offset:7120
	v_fma_f32 v14, s5, v26, v12
	v_max_f32_e32 v14, 0, v14
	v_fma_mixlo_f16 v26, v14, s2, 0
	v_accvgpr_read_b32 v25, a15
	v_fma_mixlo_f16 v14, v14, s2, -v26 op_sel_hi:[0,0,1]
	ds_write_b16 v13, v26 offset:2080
	ds_write_b16 v13, v14 offset:7200
	v_fma_f32 v14, s5, v25, v12
	v_max_f32_e32 v14, 0, v14
	v_fma_mixlo_f16 v25, v14, s2, 0
	v_accvgpr_read_b32 v24, a16
	v_fma_mixlo_f16 v14, v14, s2, -v25 op_sel_hi:[0,0,1]
	ds_write_b16 v13, v25 offset:2160
	ds_write_b16 v13, v14 offset:7280
	v_fma_f32 v14, s5, v24, v12
	v_max_f32_e32 v14, 0, v14
	v_fma_mixlo_f16 v24, v14, s2, 0
	v_accvgpr_read_b32 v23, a17
	v_fma_mixlo_f16 v14, v14, s2, -v24 op_sel_hi:[0,0,1]
	ds_write_b16 v13, v24 offset:2560
	ds_write_b16 v13, v14 offset:7680
	v_fma_f32 v14, s5, v23, v12
	v_max_f32_e32 v14, 0, v14
	v_fma_mixlo_f16 v23, v14, s2, 0
	v_accvgpr_read_b32 v22, a18
	v_fma_mixlo_f16 v14, v14, s2, -v23 op_sel_hi:[0,0,1]
	ds_write_b16 v13, v23 offset:2640
	ds_write_b16 v13, v14 offset:7760
	v_fma_f32 v14, s5, v22, v12
	v_max_f32_e32 v14, 0, v14
	v_fma_mixlo_f16 v22, v14, s2, 0
	v_accvgpr_read_b32 v21, a19
	v_fma_mixlo_f16 v14, v14, s2, -v22 op_sel_hi:[0,0,1]
	ds_write_b16 v13, v22 offset:2720
	ds_write_b16 v13, v14 offset:7840
	v_fma_f32 v14, s5, v21, v12
	v_max_f32_e32 v14, 0, v14
	v_fma_mixlo_f16 v21, v14, s2, 0
	v_accvgpr_read_b32 v20, a20
	v_fma_mixlo_f16 v14, v14, s2, -v21 op_sel_hi:[0,0,1]
	ds_write_b16 v13, v21 offset:2800
	ds_write_b16 v13, v14 offset:7920
	v_fma_f32 v14, s5, v20, v12
	v_max_f32_e32 v14, 0, v14
	v_fma_mixlo_f16 v20, v14, s2, 0
	v_accvgpr_read_b32 v19, a21
	v_fma_mixlo_f16 v14, v14, s2, -v20 op_sel_hi:[0,0,1]
	ds_write_b16 v13, v20 offset:3200
	ds_write_b16 v13, v14 offset:8320
	v_fma_f32 v14, s5, v19, v12
	v_max_f32_e32 v14, 0, v14
	v_fma_mixlo_f16 v19, v14, s2, 0
	v_accvgpr_read_b32 v18, a22
	v_fma_mixlo_f16 v14, v14, s2, -v19 op_sel_hi:[0,0,1]
	ds_write_b16 v13, v19 offset:3280
	ds_write_b16 v13, v14 offset:8400
	v_fma_f32 v14, s5, v18, v12
	v_max_f32_e32 v14, 0, v14
	v_fma_mixlo_f16 v18, v14, s2, 0
	v_accvgpr_read_b32 v17, a23
	v_fma_mixlo_f16 v14, v14, s2, -v18 op_sel_hi:[0,0,1]
	ds_write_b16 v13, v18 offset:3360
	ds_write_b16 v13, v14 offset:8480
	v_fma_f32 v14, s5, v17, v12
	v_max_f32_e32 v14, 0, v14
	v_fma_mixlo_f16 v17, v14, s2, 0
	v_accvgpr_read_b32 v16, a24
	v_fma_mixlo_f16 v14, v14, s2, -v17 op_sel_hi:[0,0,1]
	ds_write_b16 v13, v17 offset:3440
	ds_write_b16 v13, v14 offset:8560
	v_fma_f32 v14, s5, v16, v12
	v_max_f32_e32 v14, 0, v14
	v_fma_mixlo_f16 v16, v14, s2, 0
	v_accvgpr_read_b32 v15, a25
	v_fma_mixlo_f16 v14, v14, s2, -v16 op_sel_hi:[0,0,1]
	ds_write_b16 v13, v16 offset:3840
	ds_write_b16 v13, v14 offset:8960
	v_fma_f32 v14, s5, v15, v12
	v_accvgpr_read_b32 v11, a26
	v_max_f32_e32 v14, 0, v14
	v_fma_mixlo_f16 v15, v14, s2, 0
	v_fma_f32 v11, s5, v11, v12
	v_accvgpr_read_b32 v10, a27
	v_fma_mixlo_f16 v14, v14, s2, -v15 op_sel_hi:[0,0,1]
	v_max_f32_e32 v11, 0, v11
	ds_write_b16 v13, v15 offset:3920
	ds_write_b16 v13, v14 offset:9040
	v_fma_mixlo_f16 v14, v11, s2, 0
	v_fma_f32 v10, s5, v10, v12
	v_accvgpr_read_b32 v9, a28
	v_fma_mixlo_f16 v11, v11, s2, -v14 op_sel_hi:[0,0,1]
	v_max_f32_e32 v10, 0, v10
	ds_write_b16 v13, v14 offset:4000
	ds_write_b16 v13, v11 offset:9120
	v_fma_mixlo_f16 v11, v10, s2, 0
	v_fma_f32 v9, s5, v9, v12
	v_accvgpr_read_b32 v8, a29
	v_fma_mixlo_f16 v10, v10, s2, -v11 op_sel_hi:[0,0,1]
	v_max_f32_e32 v9, 0, v9
	ds_write_b16 v13, v11 offset:4080
	ds_write_b16 v13, v10 offset:9200
	v_fma_mixlo_f16 v10, v9, s2, 0
	v_fma_f32 v8, s5, v8, v12
	v_accvgpr_read_b32 v7, a30
	v_fma_mixlo_f16 v9, v9, s2, -v10 op_sel_hi:[0,0,1]
	v_max_f32_e32 v8, 0, v8
	ds_write_b16 v13, v10 offset:4480
	ds_write_b16 v13, v9 offset:9600
	v_fma_mixlo_f16 v9, v8, s2, 0
	v_fma_f32 v7, s5, v7, v12
	v_accvgpr_read_b32 v6, a31
	v_fma_mixlo_f16 v8, v8, s2, -v9 op_sel_hi:[0,0,1]
	v_max_f32_e32 v7, 0, v7
	ds_write_b16 v13, v9 offset:4560
	ds_write_b16 v13, v8 offset:9680
	v_fma_mixlo_f16 v8, v7, s2, 0
	v_fmac_f32_e32 v12, s5, v6
	v_fma_mixlo_f16 v7, v7, s2, -v8 op_sel_hi:[0,0,1]
	v_max_f32_e32 v6, 0, v12
	v_lshrrev_b32_e32 v20, 2, v3
	v_add_u32_e32 v1, s4, v1
	v_or_b32_e32 v0, v0, v2
	v_lshl_or_b32 v2, v2, 1, v41
	ds_write_b16 v13, v8 offset:4640
	ds_write_b16 v13, v7 offset:9760
	v_fma_mixlo_f16 v7, v6, s2, 0
	v_mul_u32_u24_e32 v3, 40, v20
	v_lshlrev_b64 v[4:5], 1, v[0:1]
	v_fma_mixlo_f16 v6, v6, s2, -v7 op_sel_hi:[0,0,1]
	ds_write_b16 v13, v7 offset:4720
	ds_write_b16 v13, v6 offset:9840
	v_lshl_add_u32 v21, v3, 1, v2
	v_mad_u64_u32 v[10:11], s[2:3], s0, v20, 0
	v_lshl_add_u64 v[0:1], s[8:9], 0, v[4:5]
	v_lshl_add_u64 v[14:15], s[10:11], 0, v[4:5]
	ds_read_b128 v[2:5], v21
	ds_read_b128 v[6:9], v21 offset:5120
	v_mov_b32_e32 v12, v11
	v_mad_u64_u32 v[12:13], s[2:3], s1, v20, v[12:13]
	v_mov_b32_e32 v11, v12
	v_lshlrev_b64 v[16:17], 1, v[10:11]
	v_lshl_add_u64 v[18:19], v[0:1], 0, v[16:17]
	v_lshl_add_u64 v[16:17], v[14:15], 0, v[16:17]
	s_waitcnt lgkmcnt(0)
	global_store_dwordx4 v[16:17], v[6:9], off sc1
	ds_read_b128 v[10:13], v21 offset:1280
	global_store_dwordx4 v[18:19], v[2:5], off sc1
	v_or_b32_e32 v9, 16, v20
	v_mad_u64_u32 v[6:7], s[2:3], s0, v9, 0
	v_mov_b32_e32 v8, v7
	ds_read_b128 v[2:5], v21 offset:6400
	v_mad_u64_u32 v[8:9], s[2:3], s1, v9, v[8:9]
	v_mov_b32_e32 v7, v8
	v_lshlrev_b64 v[6:7], 1, v[6:7]
	v_lshl_add_u64 v[8:9], v[0:1], 0, v[6:7]
	s_waitcnt lgkmcnt(1)
	global_store_dwordx4 v[8:9], v[10:13], off sc1
	v_lshl_add_u64 v[6:7], v[14:15], 0, v[6:7]
	s_waitcnt lgkmcnt(0)
	global_store_dwordx4 v[6:7], v[2:5], off sc1
	v_or_b32_e32 v13, 32, v20
	v_mad_u64_u32 v[10:11], s[2:3], s0, v13, 0
	ds_read_b128 v[2:5], v21 offset:2560
	ds_read_b128 v[6:9], v21 offset:7680
	v_mov_b32_e32 v12, v11
	v_mad_u64_u32 v[12:13], s[2:3], s1, v13, v[12:13]
	v_mov_b32_e32 v11, v12
	v_lshlrev_b64 v[16:17], 1, v[10:11]
	v_lshl_add_u64 v[18:19], v[0:1], 0, v[16:17]
	v_lshl_add_u64 v[16:17], v[14:15], 0, v[16:17]
	s_waitcnt lgkmcnt(0)
	global_store_dwordx4 v[16:17], v[6:9], off sc1
	ds_read_b128 v[10:13], v21 offset:3840
	global_store_dwordx4 v[18:19], v[2:5], off sc1
	v_or_b32_e32 v9, 48, v20
	v_mad_u64_u32 v[6:7], s[2:3], s0, v9, 0
	v_mov_b32_e32 v8, v7
	ds_read_b128 v[2:5], v21 offset:8960
	v_mad_u64_u32 v[8:9], s[0:1], s1, v9, v[8:9]
	v_mov_b32_e32 v7, v8
	v_lshlrev_b64 v[6:7], 1, v[6:7]
	v_lshl_add_u64 v[0:1], v[0:1], 0, v[6:7]
	s_waitcnt lgkmcnt(1)
	global_store_dwordx4 v[0:1], v[10:13], off sc1
	v_lshl_add_u64 v[0:1], v[14:15], 0, v[6:7]
	s_waitcnt lgkmcnt(0)
	global_store_dwordx4 v[0:1], v[2:5], off sc1
	s_endpgm
	s_endpgm
	s_endpgm
	s_endpgm
	s_endpgm
	s_endpgm
	s_endpgm
	s_endpgm
	s_endpgm
	s_endpgm
	s_endpgm
	s_endpgm
	s_endpgm
	s_endpgm
	s_endpgm
	s_endpgm
	s_endpgm
	s_endpgm
	s_endpgm
	s_endpgm
	s_endpgm
	s_endpgm
	s_endpgm
	s_endpgm
	s_endpgm
	s_endpgm
	s_endpgm
	s_endpgm
	s_endpgm
	s_endpgm
	s_endpgm
	s_endpgm
	s_endpgm
	s_endpgm
	s_endpgm
	s_endpgm
	s_endpgm
	s_endpgm
	s_endpgm
	s_endpgm
	s_endpgm
	s_endpgm
	s_endpgm
	s_endpgm
	s_endpgm
	s_endpgm

.LBB23_8:
	s_or_b64 exec, exec, s[18:19]
	s_mul_i32 s19, s22, s21
	s_sub_i32 s7, s7, s19
	s_xor_b32 s18, s23, s24
	s_add_i32 s19, s22, 1
	s_sub_i32 s23, s7, s21
	s_cmp_ge_u32 s7, s21
	s_cselect_b32 s19, s19, s22
	s_cselect_b32 s7, s23, s7
	s_add_i32 s22, s19, 1
	s_cmp_ge_u32 s7, s21
	s_cselect_b32 s7, s22, s19
	s_xor_b32 s7, s7, s18
	s_sub_i32 s7, s7, s18
	s_load_dwordx2 s[16:17], s[0:1], 0x10
	s_load_dword s25, s[0:1], 0x28
	s_mul_i32 s3, s7, s3
	v_lshlrev_b32_e32 v2, 3, v0
	s_mul_i32 s18, s7, s5
	s_sub_i32 s3, s20, s3
	v_lshrrev_b32_e32 v23, 2, v0
	v_and_b32_e32 v56, 24, v2
	s_ashr_i32 s19, s18, 31
	v_mov_b32_e32 v57, 0
	s_lshl_b32 s3, s3, 7
	v_lshl_add_u64 v[2:3], s[18:19], 0, v[56:57]
	v_add_u32_e32 v4, s2, v23
	s_add_i32 s18, s4, -1
	v_or_b32_e32 v6, s3, v23
	s_ashr_i32 s7, s3, 31
	v_min_i32_e32 v7, s18, v4
	v_add_u32_e32 v4, 64, v4
	v_min_i32_e32 v8, s18, v4
	s_waitcnt lgkmcnt(0)
	s_mul_i32 s7, s16, s7
	v_mad_u64_u32 v[4:5], s[18:19], s16, v6, v[2:3]
	v_mul_lo_u32 v6, s17, v6
	v_add3_u32 v5, v6, v5, s7
	v_lshlrev_b64 v[4:5], 1, v[4:5]
	v_mad_i64_i32 v[10:11], s[18:19], v7, s25, v[2:3]
	v_mad_i64_i32 v[14:15], s[18:19], v8, s25, v[2:3]
	v_lshl_add_u64 v[2:3], s[12:13], 0, v[4:5]
	global_load_dwordx4 v[126:129], v[2:3], off
	v_lshl_add_u64 v[4:5], s[14:15], 0, v[4:5]
	s_lshl_b64 s[12:13], s[16:17], 7
	global_load_dwordx4 v[130:133], v[4:5], off
	v_lshl_add_u64 v[6:7], v[2:3], 0, s[12:13]
	global_load_dwordx4 v[134:137], v[6:7], off
	v_lshl_add_u64 v[8:9], v[4:5], 0, s[12:13]
	v_lshlrev_b64 v[12:13], 1, v[10:11]
	global_load_dwordx4 v[138:141], v[8:9], off
	v_lshl_add_u64 v[10:11], s[8:9], 0, v[12:13]
	global_load_dwordx4 v[142:145], v[10:11], off
	v_lshl_add_u64 v[12:13], s[10:11], 0, v[12:13]
	v_lshlrev_b64 v[16:17], 1, v[14:15]
	global_load_dwordx4 v[146:149], v[12:13], off
	v_lshl_add_u64 v[14:15], s[8:9], 0, v[16:17]
	global_load_dwordx4 v[150:153], v[14:15], off
	v_lshl_add_u64 v[16:17], s[10:11], 0, v[16:17]
	global_load_dwordx4 v[154:157], v[16:17], off
	s_load_dwordx2 s[8:9], s[0:1], 0x38
	v_lshrrev_b32_e32 v21, 1, v0
	v_mul_u32_u24_e32 v23, 40, v23
	v_lshlrev_b32_e32 v56, 1, v56
	s_nop 7
	v_and_b32_e32 v21, 64, v21
	v_bfe_u32 v22, v0, 5, 1
	v_lshl_add_u32 v23, v23, 1, v56
	s_ashr_i32 s7, s5, 31
	s_lshr_b32 s7, s7, 27
	s_add_i32 s5, s5, s7
	s_ashr_i32 s5, s5, 5
	s_add_i32 s7, s5, -1
	s_min_i32 s10, s7, 2
	s_lshl_b32 s10, s10, 5
	s_ashr_i32 s11, s10, 31
	s_lshl_b64 s[10:11], s[10:11], 1
	v_lshl_add_u64 v[24:25], v[2:3], 0, s[10:11]
	global_load_dwordx4 v[30:33], v[2:3], off offset:64
	global_load_dwordx4 v[34:37], v[4:5], off offset:64
	global_load_dwordx4 v[42:45], v[6:7], off offset:64
	global_load_dwordx4 v[54:57], v[8:9], off offset:64
	global_load_dwordx4 v[46:49], v[10:11], off offset:64
	global_load_dwordx4 v[50:53], v[12:13], off offset:64
	global_load_dwordx4 v[58:61], v[14:15], off offset:64
	global_load_dwordx4 v[62:65], v[16:17], off offset:64
	global_load_dwordx4 v[38:41], v[24:25], off
	v_lshl_add_u64 v[24:25], v[4:5], 0, s[10:11]
	global_load_dwordx4 v[66:69], v[24:25], off
	v_lshl_add_u64 v[24:25], v[6:7], 0, s[10:11]
	global_load_dwordx4 v[70:73], v[24:25], off
	v_lshl_add_u64 v[24:25], v[8:9], 0, s[10:11]
	global_load_dwordx4 v[78:81], v[24:25], off
	v_lshl_add_u64 v[24:25], v[10:11], 0, s[10:11]
	global_load_dwordx4 v[74:77], v[24:25], off
	v_lshl_add_u64 v[24:25], v[12:13], 0, s[10:11]
	global_load_dwordx4 v[82:85], v[24:25], off
	v_lshl_add_u64 v[24:25], v[14:15], 0, s[10:11]
	global_load_dwordx4 v[86:89], v[24:25], off
	v_lshl_add_u64 v[24:25], v[16:17], 0, s[10:11]
	global_load_dwordx4 v[90:93], v[24:25], off
	v_accvgpr_write_b32 a48, 0
	v_accvgpr_write_b32 a49, 0
	v_accvgpr_write_b32 a50, 0
	v_accvgpr_write_b32 a51, 0
	v_accvgpr_write_b32 a52, 0
	v_accvgpr_write_b32 a53, 0
	v_accvgpr_write_b32 a54, 0
	v_accvgpr_write_b32 a55, 0
	v_accvgpr_write_b32 a56, 0
	v_accvgpr_write_b32 a57, 0
	v_accvgpr_write_b32 a58, 0
	v_accvgpr_write_b32 a59, 0
	v_accvgpr_write_b32 a60, 0
	v_accvgpr_write_b32 a61, 0
	v_accvgpr_write_b32 a62, 0
	v_accvgpr_write_b32 a63, 0
	v_accvgpr_write_b32 a32, 0
	v_accvgpr_write_b32 a33, 0
	v_accvgpr_write_b32 a34, 0
	v_accvgpr_write_b32 a35, 0
	v_accvgpr_write_b32 a36, 0
	v_accvgpr_write_b32 a37, 0
	v_accvgpr_write_b32 a38, 0
	v_accvgpr_write_b32 a39, 0
	v_accvgpr_write_b32 a40, 0
	v_accvgpr_write_b32 a41, 0
	v_accvgpr_write_b32 a42, 0
	v_accvgpr_write_b32 a43, 0
	v_accvgpr_write_b32 a44, 0
	v_accvgpr_write_b32 a45, 0
	v_accvgpr_write_b32 a46, 0
	v_accvgpr_write_b32 a47, 0
	v_accvgpr_write_b32 a16, 0
	v_accvgpr_write_b32 a17, 0
	v_accvgpr_write_b32 a18, 0
	v_accvgpr_write_b32 a19, 0
	v_accvgpr_write_b32 a20, 0
	v_accvgpr_write_b32 a21, 0
	v_accvgpr_write_b32 a22, 0
	v_accvgpr_write_b32 a23, 0
	v_accvgpr_write_b32 a24, 0
	v_accvgpr_write_b32 a25, 0
	v_accvgpr_write_b32 a26, 0
	v_accvgpr_write_b32 a27, 0
	v_accvgpr_write_b32 a28, 0
	v_accvgpr_write_b32 a29, 0
	v_accvgpr_write_b32 a30, 0
	v_accvgpr_write_b32 a31, 0
	v_accvgpr_write_b32 a0, 0
	v_accvgpr_write_b32 a1, 0
	v_accvgpr_write_b32 a2, 0
	v_accvgpr_write_b32 a3, 0
	v_accvgpr_write_b32 a4, 0
	v_accvgpr_write_b32 a5, 0
	v_accvgpr_write_b32 a6, 0
	v_accvgpr_write_b32 a7, 0
	v_accvgpr_write_b32 a8, 0
	v_accvgpr_write_b32 a9, 0
	v_accvgpr_write_b32 a10, 0
	v_accvgpr_write_b32 a11, 0
	v_accvgpr_write_b32 a12, 0
	v_accvgpr_write_b32 a13, 0
	v_accvgpr_write_b32 a14, 0
	v_accvgpr_write_b32 a15, 0
	s_waitcnt vmcnt(23)
	ds_write_b128 v23, v[126:129]
	s_waitcnt vmcnt(22)
	ds_write_b128 v23, v[130:133] offset:10240
	s_waitcnt vmcnt(21)
	ds_write_b128 v23, v[134:137] offset:5120
	s_waitcnt vmcnt(20)
	ds_write_b128 v23, v[138:141] offset:15360
	s_waitcnt vmcnt(19)
	ds_write_b128 v23, v[142:145] offset:20480
	s_waitcnt vmcnt(18)
	ds_write_b128 v23, v[146:149] offset:30720
	s_waitcnt vmcnt(17)
	ds_write_b128 v23, v[150:153] offset:25600
	s_waitcnt vmcnt(16)
	ds_write_b128 v23, v[154:157] offset:35840
	s_waitcnt lgkmcnt(0)
	s_barrier
	v_and_b32_e32 v27, 0x5f, v0
	v_lshlrev_b32_e32 v28, 4, v22
	s_movk_i32 s10, 0x50
	v_or_b32_e32 v26, v21, v20
	v_mad_u32_u24 v24, v27, s10, v28
	v_mad_u32_u24 v25, v26, s10, v28
	ds_read_b128 v[98:101], v24 offset:23040
	ds_read_b128 v[102:105], v24 offset:30720
	ds_read_b128 v[118:121], v25 offset:2560
	ds_read_b128 v[110:113], v25
	ds_read_b128 v[106:109], v24 offset:33280
	ds_read_b128 v[94:97], v24 offset:20480
	ds_read_b128 v[122:125], v25 offset:12800
	ds_read_b128 v[114:117], v25 offset:10240
	v_mul_u32_u24_e32 v29, 0x50, v26
	v_add_u32_e32 v25, 0xa000, v23
	v_add_u32_e32 v26, 0xa000, v24
	v_add_u32_e32 v27, 0xa020, v24
	s_nop 7
	s_mov_b32 s10, 0
	v_add_u32_e32 v28, v28, v29
